# GEMM epilogues (w_in, kv, qkv): xor-16/xor-32 lane exchanges via v_permlane16/32_swap + v_cndmask instead of ds_bpermute LDS round trips (same values)
# baseline (speedup 1.0000x reference)
.LBB0_192:
	s_lshl_b32 s43, s26, 8
	s_add_i32 s43, s43, s68
	v_or_b32_e32 v156, s43, v1
	v_lshl_or_b32 v158, s50, 8, v161
	v_mov_b64_e32 v[170:171], s[30:31]
	v_mul_f32_e32 v138, v71, v71
	v_mul_f32_e32 v169, v73, v73
	v_ashrrev_i32_e32 v159, 31, v158
	v_mad_i64_i32 v[170:171], s[52:53], v156, s73, v[170:171]
	v_fmac_f32_e32 v138, v70, v70
	v_fmac_f32_e32 v169, v72, v72
	v_lshl_add_u64 v[174:175], v[158:159], 1, v[170:171]
	v_add_f32_e32 v138, v138, v169
	v_mul_f32_e32 v169, v67, v67
	v_mul_f32_e32 v170, v69, v69
	v_fmac_f32_e32 v169, v66, v66
	v_fmac_f32_e32 v170, v68, v68
	v_add_f32_e32 v169, v169, v170
	v_add_f32_e32 v138, v138, v169
	v_mul_f32_e32 v169, v127, v127
	v_mul_f32_e32 v172, v129, v129
	v_fmac_f32_e32 v169, v126, v126
	v_fmac_f32_e32 v172, v128, v128
	v_add_f32_e32 v169, v169, v172
	v_mul_f32_e32 v172, v123, v123
	v_mul_f32_e32 v173, v125, v125
	v_fmac_f32_e32 v172, v122, v122
	v_fmac_f32_e32 v173, v124, v124
	v_add_f32_e32 v172, v172, v173
	v_add_f32_e32 v169, v169, v172
	v_and_b32_e32 v172, 64, v168
	v_add_f32_e32 v169, v138, v169
	v_xor_b32_e32 v138, 16, v168
	v_add_u32_e32 v176, 64, v172
	v_cmp_lt_i32_e32 vcc, v138, v176
	v_cvt_pk_bf16_f32 v170, v70, v71
	v_cvt_pk_bf16_f32 v171, v72, v73
	v_cvt_pk_bf16_f32 v172, v66, v67
	v_cvt_pk_bf16_f32 v173, v68, v69
	global_store_dwordx4 v[174:175], v[170:173], off
	s_nop 0
	v_cndmask_b32_e32 v138, v168, v138, vcc
	v_lshlrev_b32_e32 v138, 2, v138
	s_mov_b32 s100, 0xffff
	s_mov_b32 s101, 0xffff
	v_mov_b32_e32 v244, v169
	v_mov_b32_e32 v177, v169
	s_nop 1
	v_permlane16_swap_b32_e32 v244, v177
	v_cndmask_b32_e64 v177, v244, v177, s[100:101]
	v_cvt_pk_bf16_f32 v170, v126, v127
	v_xor_b32_e32 v126, 32, v168
	v_cmp_lt_i32_e32 vcc, v126, v176
	v_ashrrev_i32_e32 v157, 31, v156
	s_waitcnt lgkmcnt(0)
	v_add_f32_e32 v127, v169, v177
	v_cndmask_b32_e32 v126, v168, v126, vcc
	v_lshlrev_b32_e32 v126, 2, v126
	s_mov_b32 s100, -1
	s_mov_b32 s101, 0
	v_mov_b32_e32 v244, v127
	v_mov_b32_e32 v169, v127
	s_nop 1
	v_permlane32_swap_b32_e32 v244, v169
	v_cndmask_b32_e64 v169, v244, v169, s[100:101]
	v_cvt_pk_bf16_f32 v171, v128, v129
	v_cvt_pk_bf16_f32 v172, v122, v123
	v_cvt_pk_bf16_f32 v173, v124, v125
	global_store_dwordx4 v[174:175], v[170:173], off offset:256
	s_and_saveexec_b64 s[52:53], s[6:7]
	s_cbranch_execz .LBB0_194
	s_lshl_b32 s54, s50, 2
	v_mov_b64_e32 v[122:123], s[34:35]
	s_ashr_i32 s55, s54, 31
	v_mad_i64_i32 v[122:123], s[56:57], v156, s74, v[122:123]
	v_lshl_add_u64 v[122:123], s[54:55], 2, v[122:123]
	s_lshl_b32 s26, s67, 2
	s_waitcnt lgkmcnt(0)
	v_add_f32_e32 v124, v127, v169
	v_lshl_add_u64 v[122:123], v[122:123], 0, s[26:27]
	global_store_dword v[122:123], v124, off
.LBB0_194:
	s_or_b64 exec, exec, s[52:53]
	v_mul_f32_e32 v127, v55, v55
	v_mul_f32_e32 v128, v57, v57
	v_fmac_f32_e32 v127, v54, v54
	v_fmac_f32_e32 v128, v56, v56
	v_add_f32_e32 v127, v127, v128
	v_mul_f32_e32 v128, v51, v51
	v_mul_f32_e32 v129, v53, v53
	v_fmac_f32_e32 v128, v50, v50
	v_fmac_f32_e32 v129, v52, v52
	v_add_f32_e32 v128, v128, v129
	v_add_f32_e32 v127, v127, v128
	v_mul_f32_e32 v128, v119, v119
	v_mul_f32_e32 v129, v121, v121
	v_fmac_f32_e32 v128, v118, v118
	v_fmac_f32_e32 v129, v120, v120
	v_add_f32_e32 v128, v128, v129
	v_mul_f32_e32 v129, v115, v115
	s_waitcnt lgkmcnt(0)
	v_mul_f32_e32 v169, v117, v117
	v_fmac_f32_e32 v129, v114, v114
	v_fmac_f32_e32 v169, v116, v116
	v_add_f32_e32 v129, v129, v169
	v_add_f32_e32 v128, v128, v129
	v_add_f32_e32 v127, v127, v128
	s_mov_b32 s100, 0xffff
	s_mov_b32 s101, 0xffff
	v_mov_b32_e32 v244, v127
	v_mov_b32_e32 v128, v127
	s_nop 1
	v_permlane16_swap_b32_e32 v244, v128
	v_cndmask_b32_e64 v128, v244, v128, s[100:101]
	v_or_b32_e32 v122, 16, v156
	v_mov_b64_e32 v[124:125], s[30:31]
	v_mad_i64_i32 v[124:125], s[52:53], v122, s73, v[124:125]
	v_lshl_add_u64 v[124:125], v[158:159], 1, v[124:125]
	v_cvt_pk_bf16_f32 v170, v54, v55
	v_cvt_pk_bf16_f32 v171, v56, v57
	v_cvt_pk_bf16_f32 v172, v50, v51
	v_cvt_pk_bf16_f32 v173, v52, v53
	global_store_dwordx4 v[124:125], v[170:173], off
	v_ashrrev_i32_e32 v123, 31, v122
	s_nop 0
	v_cvt_pk_bf16_f32 v170, v118, v119
	s_waitcnt lgkmcnt(0)
	v_add_f32_e32 v118, v127, v128
	s_mov_b32 s100, -1
	s_mov_b32 s101, 0
	v_mov_b32_e32 v244, v118
	v_mov_b32_e32 v119, v118
	s_nop 1
	v_permlane32_swap_b32_e32 v244, v119
	v_cndmask_b32_e64 v119, v244, v119, s[100:101]
	v_cvt_pk_bf16_f32 v171, v120, v121
	v_cvt_pk_bf16_f32 v172, v114, v115
	v_cvt_pk_bf16_f32 v173, v116, v117
	global_store_dwordx4 v[124:125], v[170:173], off offset:256
	s_and_saveexec_b64 s[52:53], s[6:7]
	s_cbranch_execz .LBB0_196
	s_lshl_b32 s54, s50, 2
	v_mov_b64_e32 v[114:115], s[34:35]
	s_ashr_i32 s55, s54, 31
	v_mad_i64_i32 v[114:115], s[56:57], v122, s74, v[114:115]
	v_lshl_add_u64 v[114:115], s[54:55], 2, v[114:115]
	s_lshl_b32 s26, s67, 2
	s_waitcnt lgkmcnt(0)
	v_add_f32_e32 v116, v118, v119
	v_lshl_add_u64 v[114:115], v[114:115], 0, s[26:27]
	global_store_dword v[114:115], v116, off
.LBB0_196:
	s_or_b64 exec, exec, s[52:53]
	v_or_b32_e32 v114, 32, v156
	v_mov_b64_e32 v[116:117], s[30:31]
	v_mad_i64_i32 v[116:117], s[52:53], v114, s73, v[116:117]
	v_lshl_add_u64 v[120:121], v[158:159], 1, v[116:117]
	v_mul_f32_e32 v116, v47, v47
	v_mul_f32_e32 v117, v49, v49
	s_waitcnt lgkmcnt(0)
	v_mul_f32_e32 v119, v111, v111
	v_mul_f32_e32 v124, v113, v113
	v_fmac_f32_e32 v116, v46, v46
	v_fmac_f32_e32 v117, v48, v48
	v_fmac_f32_e32 v119, v110, v110
	v_fmac_f32_e32 v124, v112, v112
	v_add_f32_e32 v116, v116, v117
	v_mul_f32_e32 v117, v43, v43
	v_mul_f32_e32 v118, v45, v45
	v_add_f32_e32 v119, v119, v124
	v_mul_f32_e32 v124, v107, v107
	v_mul_f32_e32 v125, v109, v109
	v_fmac_f32_e32 v117, v42, v42
	v_fmac_f32_e32 v118, v44, v44
	v_fmac_f32_e32 v124, v106, v106
	v_fmac_f32_e32 v125, v108, v108
	v_add_f32_e32 v117, v117, v118
	v_add_f32_e32 v124, v124, v125
	v_add_f32_e32 v118, v116, v117
	v_add_f32_e32 v119, v119, v124
	v_add_f32_e32 v124, v118, v119
	s_mov_b32 s100, 0xffff
	s_mov_b32 s101, 0xffff
	v_mov_b32_e32 v244, v124
	v_mov_b32_e32 v125, v124
	s_nop 1
	v_permlane16_swap_b32_e32 v244, v125
	v_cndmask_b32_e64 v125, v244, v125, s[100:101]
	v_cvt_pk_bf16_f32 v116, v46, v47
	v_cvt_pk_bf16_f32 v117, v48, v49
	v_cvt_pk_bf16_f32 v118, v42, v43
	v_cvt_pk_bf16_f32 v119, v44, v45
	global_store_dwordx4 v[120:121], v[116:119], off
	v_ashrrev_i32_e32 v115, 31, v114
	s_nop 0
	v_cvt_pk_bf16_f32 v116, v110, v111
	s_waitcnt lgkmcnt(0)
	v_add_f32_e32 v110, v124, v125
	s_mov_b32 s100, -1
	s_mov_b32 s101, 0
	v_mov_b32_e32 v244, v110
	v_mov_b32_e32 v111, v110
	s_nop 1
	v_permlane32_swap_b32_e32 v244, v111
	v_cndmask_b32_e64 v111, v244, v111, s[100:101]
	v_cvt_pk_bf16_f32 v117, v112, v113
	v_cvt_pk_bf16_f32 v118, v106, v107
	v_cvt_pk_bf16_f32 v119, v108, v109
	global_store_dwordx4 v[120:121], v[116:119], off offset:256
	s_and_saveexec_b64 s[52:53], s[6:7]
	s_cbranch_execz .LBB0_198
	s_lshl_b32 s54, s50, 2
	v_mov_b64_e32 v[106:107], s[34:35]
	s_ashr_i32 s55, s54, 31
	v_mad_i64_i32 v[106:107], s[56:57], v114, s74, v[106:107]
	v_lshl_add_u64 v[106:107], s[54:55], 2, v[106:107]
	s_lshl_b32 s26, s67, 2
	s_waitcnt lgkmcnt(0)
	v_add_f32_e32 v108, v110, v111
	v_lshl_add_u64 v[106:107], v[106:107], 0, s[26:27]
	global_store_dword v[106:107], v108, off
.LBB0_198:
	s_or_b64 exec, exec, s[52:53]
	v_or_b32_e32 v106, 48, v156
	v_mov_b64_e32 v[108:109], s[30:31]
	v_mad_i64_i32 v[108:109], s[52:53], v106, s73, v[108:109]
	v_lshl_add_u64 v[112:113], v[158:159], 1, v[108:109]
	v_mul_f32_e32 v108, v39, v39
	v_mul_f32_e32 v109, v41, v41
	s_waitcnt lgkmcnt(0)
	v_mul_f32_e32 v111, v103, v103
	v_mul_f32_e32 v116, v105, v105
	v_fmac_f32_e32 v108, v38, v38
	v_fmac_f32_e32 v109, v40, v40
	v_fmac_f32_e32 v111, v102, v102
	v_fmac_f32_e32 v116, v104, v104
	v_add_f32_e32 v108, v108, v109
	v_mul_f32_e32 v109, v35, v35
	v_mul_f32_e32 v110, v37, v37
	v_add_f32_e32 v111, v111, v116
	v_mul_f32_e32 v116, v99, v99
	v_mul_f32_e32 v117, v101, v101
	v_fmac_f32_e32 v109, v34, v34
	v_fmac_f32_e32 v110, v36, v36
	v_fmac_f32_e32 v116, v98, v98
	v_fmac_f32_e32 v117, v100, v100
	v_add_f32_e32 v109, v109, v110
	v_add_f32_e32 v116, v116, v117
	v_add_f32_e32 v110, v108, v109
	v_add_f32_e32 v111, v111, v116
	v_add_f32_e32 v116, v110, v111
	s_mov_b32 s100, 0xffff
	s_mov_b32 s101, 0xffff
	v_mov_b32_e32 v244, v116
	v_mov_b32_e32 v117, v116
	s_nop 1
	v_permlane16_swap_b32_e32 v244, v117
	v_cndmask_b32_e64 v117, v244, v117, s[100:101]
	v_cvt_pk_bf16_f32 v108, v38, v39
	v_cvt_pk_bf16_f32 v109, v40, v41
	v_cvt_pk_bf16_f32 v110, v34, v35
	v_cvt_pk_bf16_f32 v111, v36, v37
	global_store_dwordx4 v[112:113], v[108:111], off
	v_ashrrev_i32_e32 v107, 31, v106
	s_nop 0
	v_cvt_pk_bf16_f32 v108, v102, v103
	s_waitcnt lgkmcnt(0)
	v_add_f32_e32 v102, v116, v117
	s_mov_b32 s100, -1
	s_mov_b32 s101, 0
	v_mov_b32_e32 v244, v102
	v_mov_b32_e32 v103, v102
	s_nop 1
	v_permlane32_swap_b32_e32 v244, v103
	v_cndmask_b32_e64 v103, v244, v103, s[100:101]
	v_cvt_pk_bf16_f32 v109, v104, v105
	v_cvt_pk_bf16_f32 v110, v98, v99
	v_cvt_pk_bf16_f32 v111, v100, v101
	global_store_dwordx4 v[112:113], v[108:111], off offset:256
	s_and_saveexec_b64 s[52:53], s[6:7]
	s_cbranch_execz .LBB0_200
	s_lshl_b32 s54, s50, 2
	v_mov_b64_e32 v[98:99], s[34:35]
	s_ashr_i32 s55, s54, 31
	v_mad_i64_i32 v[98:99], s[56:57], v106, s74, v[98:99]
	v_lshl_add_u64 v[98:99], s[54:55], 2, v[98:99]
	s_lshl_b32 s26, s67, 2
	s_waitcnt lgkmcnt(0)
	v_add_f32_e32 v100, v102, v103
	v_lshl_add_u64 v[98:99], v[98:99], 0, s[26:27]
	global_store_dword v[98:99], v100, off
.LBB0_200:
	s_or_b64 exec, exec, s[52:53]
	v_add_u32_e32 v98, 0x80, v156
	v_mov_b64_e32 v[100:101], s[30:31]
	v_mad_i64_i32 v[100:101], s[52:53], v98, s73, v[100:101]
	v_lshl_add_u64 v[104:105], v[158:159], 1, v[100:101]
	v_mul_f32_e32 v100, v31, v31
	v_mul_f32_e32 v101, v33, v33
	s_waitcnt lgkmcnt(0)
	v_mul_f32_e32 v103, v95, v95
	v_mul_f32_e32 v108, v97, v97
	v_fmac_f32_e32 v100, v30, v30
	v_fmac_f32_e32 v101, v32, v32
	v_fmac_f32_e32 v103, v94, v94
	v_fmac_f32_e32 v108, v96, v96
	v_add_f32_e32 v100, v100, v101
	v_mul_f32_e32 v101, v27, v27
	v_mul_f32_e32 v102, v29, v29
	v_add_f32_e32 v103, v103, v108
	v_mul_f32_e32 v108, v91, v91
	v_mul_f32_e32 v109, v93, v93
	v_fmac_f32_e32 v101, v26, v26
	v_fmac_f32_e32 v102, v28, v28
	v_fmac_f32_e32 v108, v90, v90
	v_fmac_f32_e32 v109, v92, v92
	v_add_f32_e32 v101, v101, v102
	v_add_f32_e32 v108, v108, v109
	v_add_f32_e32 v102, v100, v101
	v_add_f32_e32 v103, v103, v108
	v_add_f32_e32 v108, v102, v103
	s_mov_b32 s100, 0xffff
	s_mov_b32 s101, 0xffff
	v_mov_b32_e32 v244, v108
	v_mov_b32_e32 v109, v108
	s_nop 1
	v_permlane16_swap_b32_e32 v244, v109
	v_cndmask_b32_e64 v109, v244, v109, s[100:101]
	v_cvt_pk_bf16_f32 v100, v30, v31
	v_cvt_pk_bf16_f32 v101, v32, v33
	v_cvt_pk_bf16_f32 v102, v26, v27
	v_cvt_pk_bf16_f32 v103, v28, v29
	global_store_dwordx4 v[104:105], v[100:103], off
	v_ashrrev_i32_e32 v99, 31, v98
	s_nop 0
	v_cvt_pk_bf16_f32 v100, v94, v95
	s_waitcnt lgkmcnt(0)
	v_add_f32_e32 v94, v108, v109
	s_mov_b32 s100, -1
	s_mov_b32 s101, 0
	v_mov_b32_e32 v244, v94
	v_mov_b32_e32 v95, v94
	s_nop 1
	v_permlane32_swap_b32_e32 v244, v95
	v_cndmask_b32_e64 v95, v244, v95, s[100:101]
	v_cvt_pk_bf16_f32 v101, v96, v97
	v_cvt_pk_bf16_f32 v102, v90, v91
	v_cvt_pk_bf16_f32 v103, v92, v93
	global_store_dwordx4 v[104:105], v[100:103], off offset:256
	s_and_saveexec_b64 s[52:53], s[6:7]
	s_cbranch_execz .LBB0_202
	s_lshl_b32 s54, s50, 2
	v_mov_b64_e32 v[90:91], s[34:35]
	s_ashr_i32 s55, s54, 31
	v_mad_i64_i32 v[90:91], s[56:57], v98, s74, v[90:91]
	v_lshl_add_u64 v[90:91], s[54:55], 2, v[90:91]
	s_lshl_b32 s26, s67, 2
	s_waitcnt lgkmcnt(0)
	v_add_f32_e32 v92, v94, v95
	v_lshl_add_u64 v[90:91], v[90:91], 0, s[26:27]
	global_store_dword v[90:91], v92, off
.LBB0_202:
	s_or_b64 exec, exec, s[52:53]
	v_add_u32_e32 v90, 0x90, v156
	v_mov_b64_e32 v[92:93], s[30:31]
	v_mad_i64_i32 v[92:93], s[52:53], v90, s73, v[92:93]
	v_lshl_add_u64 v[96:97], v[158:159], 1, v[92:93]
	v_mul_f32_e32 v92, v23, v23
	v_mul_f32_e32 v93, v25, v25
	s_waitcnt lgkmcnt(0)
	v_mul_f32_e32 v95, v87, v87
	v_mul_f32_e32 v100, v89, v89
	v_fmac_f32_e32 v92, v22, v22
	v_fmac_f32_e32 v93, v24, v24
	v_fmac_f32_e32 v95, v86, v86
	v_fmac_f32_e32 v100, v88, v88
	v_add_f32_e32 v92, v92, v93
	v_mul_f32_e32 v93, v19, v19
	v_mul_f32_e32 v94, v21, v21
	v_add_f32_e32 v95, v95, v100
	v_mul_f32_e32 v100, v83, v83
	v_mul_f32_e32 v101, v85, v85
	v_fmac_f32_e32 v93, v18, v18
	v_fmac_f32_e32 v94, v20, v20
	v_fmac_f32_e32 v100, v82, v82
	v_fmac_f32_e32 v101, v84, v84
	v_add_f32_e32 v93, v93, v94
	v_add_f32_e32 v100, v100, v101
	v_add_f32_e32 v94, v92, v93
	v_add_f32_e32 v95, v95, v100
	v_add_f32_e32 v100, v94, v95
	s_mov_b32 s100, 0xffff
	s_mov_b32 s101, 0xffff
	v_mov_b32_e32 v244, v100
	v_mov_b32_e32 v101, v100
	s_nop 1
	v_permlane16_swap_b32_e32 v244, v101
	v_cndmask_b32_e64 v101, v244, v101, s[100:101]
	v_cvt_pk_bf16_f32 v92, v22, v23
	v_cvt_pk_bf16_f32 v93, v24, v25
	v_cvt_pk_bf16_f32 v94, v18, v19
	v_cvt_pk_bf16_f32 v95, v20, v21
	global_store_dwordx4 v[96:97], v[92:95], off
	v_ashrrev_i32_e32 v91, 31, v90
	s_nop 0
	v_cvt_pk_bf16_f32 v92, v86, v87
	s_waitcnt lgkmcnt(0)
	v_add_f32_e32 v86, v100, v101
	s_mov_b32 s100, -1
	s_mov_b32 s101, 0
	v_mov_b32_e32 v244, v86
	v_mov_b32_e32 v87, v86
	s_nop 1
	v_permlane32_swap_b32_e32 v244, v87
	v_cndmask_b32_e64 v87, v244, v87, s[100:101]
	v_cvt_pk_bf16_f32 v93, v88, v89
	v_cvt_pk_bf16_f32 v94, v82, v83
	v_cvt_pk_bf16_f32 v95, v84, v85
	global_store_dwordx4 v[96:97], v[92:95], off offset:256
	s_and_saveexec_b64 s[52:53], s[6:7]
	s_cbranch_execz .LBB0_204
	s_lshl_b32 s54, s50, 2
	v_mov_b64_e32 v[82:83], s[34:35]
	s_ashr_i32 s55, s54, 31
	v_mad_i64_i32 v[82:83], s[56:57], v90, s74, v[82:83]
	v_lshl_add_u64 v[82:83], s[54:55], 2, v[82:83]
	s_lshl_b32 s26, s67, 2
	s_waitcnt lgkmcnt(0)
	v_add_f32_e32 v84, v86, v87
	v_lshl_add_u64 v[82:83], v[82:83], 0, s[26:27]
	global_store_dword v[82:83], v84, off
.LBB0_204:
	s_or_b64 exec, exec, s[52:53]
	v_add_u32_e32 v82, 0xa0, v156
	v_mov_b64_e32 v[84:85], s[30:31]
	v_mad_i64_i32 v[84:85], s[52:53], v82, s73, v[84:85]
	v_lshl_add_u64 v[88:89], v[158:159], 1, v[84:85]
	v_mul_f32_e32 v84, v15, v15
	v_mul_f32_e32 v85, v17, v17
	s_waitcnt lgkmcnt(0)
	v_mul_f32_e32 v87, v79, v79
	v_mul_f32_e32 v92, v81, v81
	v_fmac_f32_e32 v84, v14, v14
	v_fmac_f32_e32 v85, v16, v16
	v_fmac_f32_e32 v87, v78, v78
	v_fmac_f32_e32 v92, v80, v80
	v_add_f32_e32 v84, v84, v85
	v_mul_f32_e32 v85, v11, v11
	v_mul_f32_e32 v86, v13, v13
	v_add_f32_e32 v87, v87, v92
	v_mul_f32_e32 v92, v75, v75
	v_mul_f32_e32 v93, v77, v77
	v_fmac_f32_e32 v85, v10, v10
	v_fmac_f32_e32 v86, v12, v12
	v_fmac_f32_e32 v92, v74, v74
	v_fmac_f32_e32 v93, v76, v76
	v_add_f32_e32 v85, v85, v86
	v_add_f32_e32 v92, v92, v93
	v_add_f32_e32 v86, v84, v85
	v_add_f32_e32 v87, v87, v92
	v_add_f32_e32 v92, v86, v87
	s_mov_b32 s100, 0xffff
	s_mov_b32 s101, 0xffff
	v_mov_b32_e32 v244, v92
	v_mov_b32_e32 v93, v92
	s_nop 1
	v_permlane16_swap_b32_e32 v244, v93
	v_cndmask_b32_e64 v93, v244, v93, s[100:101]
	v_cvt_pk_bf16_f32 v84, v14, v15
	v_cvt_pk_bf16_f32 v85, v16, v17
	v_cvt_pk_bf16_f32 v86, v10, v11
	v_cvt_pk_bf16_f32 v87, v12, v13
	global_store_dwordx4 v[88:89], v[84:87], off
	v_ashrrev_i32_e32 v83, 31, v82
	s_nop 0
	v_cvt_pk_bf16_f32 v84, v78, v79
	s_waitcnt lgkmcnt(0)
	v_add_f32_e32 v78, v92, v93
	s_mov_b32 s100, -1
	s_mov_b32 s101, 0
	v_mov_b32_e32 v244, v78
	v_mov_b32_e32 v79, v78
	s_nop 1
	v_permlane32_swap_b32_e32 v244, v79
	v_cndmask_b32_e64 v79, v244, v79, s[100:101]
	v_cvt_pk_bf16_f32 v85, v80, v81
	v_cvt_pk_bf16_f32 v86, v74, v75
	v_cvt_pk_bf16_f32 v87, v76, v77
	global_store_dwordx4 v[88:89], v[84:87], off offset:256
	s_and_saveexec_b64 s[52:53], s[6:7]
	s_cbranch_execz .LBB0_206
	s_lshl_b32 s54, s50, 2
	v_mov_b64_e32 v[74:75], s[34:35]
	s_ashr_i32 s55, s54, 31
	v_mad_i64_i32 v[74:75], s[56:57], v82, s74, v[74:75]
	v_lshl_add_u64 v[74:75], s[54:55], 2, v[74:75]
	s_lshl_b32 s26, s67, 2
	s_waitcnt lgkmcnt(0)
	v_add_f32_e32 v76, v78, v79
	v_lshl_add_u64 v[74:75], v[74:75], 0, s[26:27]
	global_store_dword v[74:75], v76, off
.LBB0_206:
	s_or_b64 exec, exec, s[52:53]
	v_add_u32_e32 v74, 0xb0, v156
	v_mov_b64_e32 v[76:77], s[30:31]
	v_mad_i64_i32 v[76:77], s[52:53], v74, s73, v[76:77]
	v_lshl_add_u64 v[80:81], v[158:159], 1, v[76:77]
	v_mul_f32_e32 v76, v7, v7
	v_mul_f32_e32 v77, v9, v9
	s_waitcnt lgkmcnt(0)
	v_mul_f32_e32 v79, v63, v63
	v_mul_f32_e32 v84, v65, v65
	v_fmac_f32_e32 v76, v6, v6
	v_fmac_f32_e32 v77, v8, v8
	v_fmac_f32_e32 v79, v62, v62
	v_fmac_f32_e32 v84, v64, v64
	v_add_f32_e32 v76, v76, v77
	v_mul_f32_e32 v77, v3, v3
	v_mul_f32_e32 v78, v5, v5
	v_add_f32_e32 v79, v79, v84
	v_mul_f32_e32 v84, v59, v59
	v_mul_f32_e32 v85, v61, v61
	v_fmac_f32_e32 v77, v2, v2
	v_fmac_f32_e32 v78, v4, v4
	v_fmac_f32_e32 v84, v58, v58
	v_fmac_f32_e32 v85, v60, v60
	v_add_f32_e32 v77, v77, v78
	v_add_f32_e32 v84, v84, v85
	v_add_f32_e32 v78, v76, v77
	v_add_f32_e32 v79, v79, v84
	v_add_f32_e32 v84, v78, v79
	s_mov_b32 s100, 0xffff
	s_mov_b32 s101, 0xffff
	v_mov_b32_e32 v244, v84
	v_mov_b32_e32 v85, v84
	s_nop 1
	v_permlane16_swap_b32_e32 v244, v85
	v_cndmask_b32_e64 v85, v244, v85, s[100:101]
	v_cvt_pk_bf16_f32 v76, v6, v7
	v_cvt_pk_bf16_f32 v77, v8, v9
	v_cvt_pk_bf16_f32 v78, v2, v3
	v_cvt_pk_bf16_f32 v79, v4, v5
	global_store_dwordx4 v[80:81], v[76:79], off
	v_ashrrev_i32_e32 v75, 31, v74
	s_nop 0
	v_cvt_pk_bf16_f32 v76, v62, v63
	s_waitcnt lgkmcnt(0)
	v_add_f32_e32 v62, v84, v85
	s_mov_b32 s100, -1
	s_mov_b32 s101, 0
	v_mov_b32_e32 v244, v62
	v_mov_b32_e32 v63, v62
	s_nop 1
	v_permlane32_swap_b32_e32 v244, v63
	v_cndmask_b32_e64 v63, v244, v63, s[100:101]
	v_cvt_pk_bf16_f32 v77, v64, v65
	v_cvt_pk_bf16_f32 v78, v58, v59
	v_cvt_pk_bf16_f32 v79, v60, v61
	global_store_dwordx4 v[80:81], v[76:79], off offset:256
	s_and_saveexec_b64 s[52:53], s[6:7]
	s_cbranch_execz .LBB0_208
	s_lshl_b32 s54, s50, 2
	v_mov_b64_e32 v[58:59], s[34:35]
	s_ashr_i32 s55, s54, 31
	v_mad_i64_i32 v[58:59], s[56:57], v74, s74, v[58:59]
	v_lshl_add_u64 v[58:59], s[54:55], 2, v[58:59]
	s_lshl_b32 s26, s67, 2
	s_waitcnt lgkmcnt(0)
	v_add_f32_e32 v60, v62, v63
	v_lshl_add_u64 v[58:59], v[58:59], 0, s[26:27]
	global_store_dword v[58:59], v60, off
.LBB0_208:
	s_or_b64 exec, exec, s[52:53]
	s_cmp_eq_u32 s50, 4
	s_cselect_b64 s[50:51], -1, 0
	s_and_b64 s[50:51], s[50:51], s[40:41]
	s_andn2_b64 vcc, exec, s[50:51]
	s_cbranch_vccnz .LBB0_226
	s_waitcnt lgkmcnt(0)
	global_load_dwordx4 v[62:65], v[144:145], off offset:512
	global_load_dwordx4 v[58:61], v[144:145], off offset:528
	s_bfe_u32 s26, s43, 0x80006
	v_cmp_gt_i32_e32 vcc, s64, v156
	s_waitcnt vmcnt(0)
	v_pk_mul_f32 v[72:73], v[72:73], v[64:65]
	v_pk_mul_f32 v[70:71], v[70:71], v[62:63]
	v_pk_mul_f32 v[68:69], v[68:69], v[60:61]
	v_pk_mul_f32 v[66:67], v[66:67], v[58:59]
	s_mov_b32 s100, -1
	s_mov_b32 s101, 0
	v_mov_b32_e32 v244, v70
	v_mov_b32_e32 v80, v70
	s_nop 1
	v_permlane32_swap_b32_e32 v244, v80
	v_cndmask_b32_e64 v80, v244, v80, s[100:101]
	s_mov_b32 s100, -1
	s_mov_b32 s101, 0
	v_mov_b32_e32 v244, v66
	v_mov_b32_e32 v76, v66
	s_nop 1
	v_permlane32_swap_b32_e32 v244, v76
	v_cndmask_b32_e64 v76, v244, v76, s[100:101]
	s_mov_b32 s100, -1
	s_mov_b32 s101, 0
	v_mov_b32_e32 v244, v71
	v_mov_b32_e32 v81, v71
	s_nop 1
	v_permlane32_swap_b32_e32 v244, v81
	v_cndmask_b32_e64 v81, v244, v81, s[100:101]
	s_mov_b32 s100, -1
	s_mov_b32 s101, 0
	v_mov_b32_e32 v244, v67
	v_mov_b32_e32 v77, v67
	s_nop 1
	v_permlane32_swap_b32_e32 v244, v77
	v_cndmask_b32_e64 v77, v244, v77, s[100:101]
	s_mov_b32 s100, -1
	s_mov_b32 s101, 0
	v_mov_b32_e32 v244, v72
	v_mov_b32_e32 v84, v72
	s_nop 1
	v_permlane32_swap_b32_e32 v244, v84
	v_cndmask_b32_e64 v84, v244, v84, s[100:101]
	s_mov_b32 s100, -1
	s_mov_b32 s101, 0
	v_mov_b32_e32 v244, v68
	v_mov_b32_e32 v78, v68
	s_nop 1
	v_permlane32_swap_b32_e32 v244, v78
	v_cndmask_b32_e64 v78, v244, v78, s[100:101]
	s_mov_b32 s100, -1
	s_mov_b32 s101, 0
	v_mov_b32_e32 v244, v73
	v_mov_b32_e32 v85, v73
	s_nop 1
	v_permlane32_swap_b32_e32 v244, v85
	v_cndmask_b32_e64 v85, v244, v85, s[100:101]
	s_mov_b32 s100, -1
	s_mov_b32 s101, 0
	v_mov_b32_e32 v244, v69
	v_mov_b32_e32 v79, v69
	s_nop 1
	v_permlane32_swap_b32_e32 v244, v79
	v_cndmask_b32_e64 v79, v244, v79, s[100:101]
	s_and_saveexec_b64 s[50:51], vcc
	s_cbranch_execz .LBB0_211
	v_mov_b32_e32 v86, s26
	v_cndmask_b32_e64 v86, v1, v86, s[10:11]
	v_lshlrev_b32_e32 v138, 6, v86
	v_lshl_add_u64 v[92:93], v[146:147], 0, v[138:139]
	global_load_dwordx4 v[86:89], v[92:93], off
	s_nop 0
	global_load_dwordx4 v[92:95], v[92:93], off offset:16
	v_lshl_add_u64 v[96:97], v[140:141], 0, v[138:139]
	global_load_dwordx4 v[100:103], v[96:97], off
	global_load_dwordx4 v[108:111], v[96:97], off offset:16
	s_waitcnt vmcnt(3) lgkmcnt(1)
	v_pk_mul_f32 v[84:85], v[88:89], v[84:85]
	v_pk_mul_f32 v[80:81], v[86:87], v[80:81]
	s_waitcnt vmcnt(2) lgkmcnt(0)
	v_pk_mul_f32 v[78:79], v[94:95], v[78:79]
	v_pk_mul_f32 v[76:77], v[92:93], v[76:77]
	v_xor_b32_e32 v86, 0x80000000, v84
	v_xor_b32_e32 v87, 0x80000000, v85
	v_xor_b32_e32 v88, 0x80000000, v80
	v_xor_b32_e32 v89, 0x80000000, v81
	v_xor_b32_e32 v92, 0x80000000, v78
	v_xor_b32_e32 v93, 0x80000000, v79
	v_xor_b32_e32 v94, 0x80000000, v76
	v_xor_b32_e32 v95, 0x80000000, v77
	v_cndmask_b32_e64 v85, v85, v87, s[8:9]
	v_cndmask_b32_e64 v84, v84, v86, s[8:9]
	v_cndmask_b32_e64 v81, v81, v89, s[8:9]
	v_cndmask_b32_e64 v80, v80, v88, s[8:9]
	v_cndmask_b32_e64 v79, v79, v93, s[8:9]
	v_cndmask_b32_e64 v78, v78, v92, s[8:9]
	v_cndmask_b32_e64 v77, v77, v95, s[8:9]
	v_cndmask_b32_e64 v76, v76, v94, s[8:9]
	s_waitcnt vmcnt(1)
	v_pk_fma_f32 v[72:73], v[72:73], v[102:103], v[84:85]
	v_pk_fma_f32 v[70:71], v[70:71], v[100:101], v[80:81]
	s_waitcnt vmcnt(0)
	v_pk_fma_f32 v[68:69], v[68:69], v[110:111], v[78:79]
	v_pk_fma_f32 v[66:67], v[66:67], v[108:109], v[76:77]
.LBB0_211:
	s_or_b64 exec, exec, s[50:51]
	v_pk_mul_f32 v[56:57], v[56:57], v[64:65]
	v_pk_mul_f32 v[54:55], v[54:55], v[62:63]
	v_pk_mul_f32 v[52:53], v[52:53], v[60:61]
	v_pk_mul_f32 v[50:51], v[50:51], v[58:59]
	s_waitcnt lgkmcnt(7)
	s_mov_b32 s100, -1
	s_mov_b32 s101, 0
	v_mov_b32_e32 v244, v54
	v_mov_b32_e32 v80, v54
	s_nop 1
	v_permlane32_swap_b32_e32 v244, v80
	v_cndmask_b32_e64 v80, v244, v80, s[100:101]
	s_waitcnt lgkmcnt(7)
	s_mov_b32 s100, -1
	s_mov_b32 s101, 0
	v_mov_b32_e32 v244, v50
	v_mov_b32_e32 v76, v50
	s_nop 1
	v_permlane32_swap_b32_e32 v244, v76
	v_cndmask_b32_e64 v76, v244, v76, s[100:101]
	s_waitcnt lgkmcnt(7)
	s_mov_b32 s100, -1
	s_mov_b32 s101, 0
	v_mov_b32_e32 v244, v55
	v_mov_b32_e32 v81, v55
	s_nop 1
	v_permlane32_swap_b32_e32 v244, v81
	v_cndmask_b32_e64 v81, v244, v81, s[100:101]
	s_waitcnt lgkmcnt(7)
	s_mov_b32 s100, -1
	s_mov_b32 s101, 0
	v_mov_b32_e32 v244, v51
	v_mov_b32_e32 v77, v51
	s_nop 1
	v_permlane32_swap_b32_e32 v244, v77
	v_cndmask_b32_e64 v77, v244, v77, s[100:101]
	s_waitcnt lgkmcnt(7)
	s_mov_b32 s100, -1
	s_mov_b32 s101, 0
	v_mov_b32_e32 v244, v56
	v_mov_b32_e32 v84, v56
	s_nop 1
	v_permlane32_swap_b32_e32 v244, v84
	v_cndmask_b32_e64 v84, v244, v84, s[100:101]
	s_waitcnt lgkmcnt(7)
	s_mov_b32 s100, -1
	s_mov_b32 s101, 0
	v_mov_b32_e32 v244, v52
	v_mov_b32_e32 v78, v52
	s_nop 1
	v_permlane32_swap_b32_e32 v244, v78
	v_cndmask_b32_e64 v78, v244, v78, s[100:101]
	s_waitcnt lgkmcnt(7)
	s_mov_b32 s100, -1
	s_mov_b32 s101, 0
	v_mov_b32_e32 v244, v57
	v_mov_b32_e32 v85, v57
	s_nop 1
	v_permlane32_swap_b32_e32 v244, v85
	v_cndmask_b32_e64 v85, v244, v85, s[100:101]
	s_waitcnt lgkmcnt(7)
	s_mov_b32 s100, -1
	s_mov_b32 s101, 0
	v_mov_b32_e32 v244, v53
	v_mov_b32_e32 v79, v53
	s_nop 1
	v_permlane32_swap_b32_e32 v244, v79
	v_cndmask_b32_e64 v79, v244, v79, s[100:101]
	v_lshlrev_b64 v[86:87], 8, v[156:157]
	v_lshl_add_u64 v[86:87], v[142:143], 0, v[86:87]
	v_cmp_gt_i32_e32 vcc, s64, v122
	global_store_dwordx4 v[86:87], v[70:73], off
	global_store_dwordx4 v[86:87], v[66:69], off offset:16
	s_and_saveexec_b64 s[50:51], vcc
	s_cbranch_execz .LBB0_213
	v_mov_b32_e32 v66, s26
	v_cndmask_b32_e64 v66, v162, v66, s[10:11]
	v_lshlrev_b32_e32 v138, 6, v66
	v_lshl_add_u64 v[70:71], v[146:147], 0, v[138:139]
	global_load_dwordx4 v[66:69], v[70:71], off
	s_nop 0
	global_load_dwordx4 v[70:73], v[70:71], off offset:16
	v_lshl_add_u64 v[92:93], v[140:141], 0, v[138:139]
	global_load_dwordx4 v[86:89], v[92:93], off
	s_nop 0
	global_load_dwordx4 v[92:95], v[92:93], off offset:16
	s_waitcnt vmcnt(3) lgkmcnt(1)
	v_pk_mul_f32 v[68:69], v[68:69], v[84:85]
	v_pk_mul_f32 v[66:67], v[66:67], v[80:81]
	s_waitcnt vmcnt(2) lgkmcnt(0)
	v_pk_mul_f32 v[72:73], v[72:73], v[78:79]
	v_pk_mul_f32 v[70:71], v[70:71], v[76:77]
	v_xor_b32_e32 v76, 0x80000000, v68
	v_xor_b32_e32 v77, 0x80000000, v69
	v_xor_b32_e32 v78, 0x80000000, v66
	v_xor_b32_e32 v79, 0x80000000, v67
	v_xor_b32_e32 v80, 0x80000000, v72
	v_xor_b32_e32 v81, 0x80000000, v73
	v_xor_b32_e32 v84, 0x80000000, v70
	v_xor_b32_e32 v85, 0x80000000, v71
	v_cndmask_b32_e64 v69, v69, v77, s[8:9]
	v_cndmask_b32_e64 v68, v68, v76, s[8:9]
	v_cndmask_b32_e64 v67, v67, v79, s[8:9]
	v_cndmask_b32_e64 v66, v66, v78, s[8:9]
	v_cndmask_b32_e64 v73, v73, v81, s[8:9]
	v_cndmask_b32_e64 v72, v72, v80, s[8:9]
	v_cndmask_b32_e64 v71, v71, v85, s[8:9]
	v_cndmask_b32_e64 v70, v70, v84, s[8:9]
	s_waitcnt vmcnt(1)
	v_pk_fma_f32 v[56:57], v[56:57], v[88:89], v[68:69]
	v_pk_fma_f32 v[54:55], v[54:55], v[86:87], v[66:67]
	s_waitcnt vmcnt(0)
	v_pk_fma_f32 v[52:53], v[52:53], v[94:95], v[72:73]
	v_pk_fma_f32 v[50:51], v[50:51], v[92:93], v[70:71]
.LBB0_213:
	s_or_b64 exec, exec, s[50:51]
	v_pk_mul_f32 v[48:49], v[48:49], v[64:65]
	v_pk_mul_f32 v[46:47], v[46:47], v[62:63]
	v_pk_mul_f32 v[44:45], v[44:45], v[60:61]
	v_pk_mul_f32 v[42:43], v[42:43], v[58:59]
	s_mov_b32 s100, -1
	s_mov_b32 s101, 0
	v_mov_b32_e32 v244, v46
	v_mov_b32_e32 v70, v46
	s_nop 1
	v_permlane32_swap_b32_e32 v244, v70
	v_cndmask_b32_e64 v70, v244, v70, s[100:101]
	s_mov_b32 s100, -1
	s_mov_b32 s101, 0
	v_mov_b32_e32 v244, v42
	v_mov_b32_e32 v66, v42
	s_nop 1
	v_permlane32_swap_b32_e32 v244, v66
	v_cndmask_b32_e64 v66, v244, v66, s[100:101]
	s_mov_b32 s100, -1
	s_mov_b32 s101, 0
	v_mov_b32_e32 v244, v47
	v_mov_b32_e32 v71, v47
	s_nop 1
	v_permlane32_swap_b32_e32 v244, v71
	v_cndmask_b32_e64 v71, v244, v71, s[100:101]
	s_mov_b32 s100, -1
	s_mov_b32 s101, 0
	v_mov_b32_e32 v244, v43
	v_mov_b32_e32 v67, v43
	s_nop 1
	v_permlane32_swap_b32_e32 v244, v67
	v_cndmask_b32_e64 v67, v244, v67, s[100:101]
	s_mov_b32 s100, -1
	s_mov_b32 s101, 0
	v_mov_b32_e32 v244, v48
	v_mov_b32_e32 v72, v48
	s_nop 1
	v_permlane32_swap_b32_e32 v244, v72
	v_cndmask_b32_e64 v72, v244, v72, s[100:101]
	s_mov_b32 s100, -1
	s_mov_b32 s101, 0
	v_mov_b32_e32 v244, v44
	v_mov_b32_e32 v68, v44
	s_nop 1
	v_permlane32_swap_b32_e32 v244, v68
	v_cndmask_b32_e64 v68, v244, v68, s[100:101]
	s_mov_b32 s100, -1
	s_mov_b32 s101, 0
	v_mov_b32_e32 v244, v49
	v_mov_b32_e32 v73, v49
	s_nop 1
	v_permlane32_swap_b32_e32 v244, v73
	v_cndmask_b32_e64 v73, v244, v73, s[100:101]
	s_mov_b32 s100, -1
	s_mov_b32 s101, 0
	v_mov_b32_e32 v244, v45
	v_mov_b32_e32 v69, v45
	s_nop 1
	v_permlane32_swap_b32_e32 v244, v69
	v_cndmask_b32_e64 v69, v244, v69, s[100:101]
	s_waitcnt lgkmcnt(12)
	v_lshlrev_b64 v[76:77], 8, v[122:123]
	v_lshl_add_u64 v[76:77], v[142:143], 0, v[76:77]
	v_cmp_gt_i32_e32 vcc, s64, v114
	global_store_dwordx4 v[76:77], v[54:57], off
	global_store_dwordx4 v[76:77], v[50:53], off offset:16
	s_and_saveexec_b64 s[50:51], vcc
	s_cbranch_execz .LBB0_215
	v_mov_b32_e32 v50, s26
	v_cndmask_b32_e64 v50, v163, v50, s[10:11]
	v_lshlrev_b32_e32 v138, 6, v50
	v_lshl_add_u64 v[54:55], v[146:147], 0, v[138:139]
	global_load_dwordx4 v[50:53], v[54:55], off
	s_nop 0
	global_load_dwordx4 v[54:57], v[54:55], off offset:16
	v_lshl_add_u64 v[80:81], v[140:141], 0, v[138:139]
	s_waitcnt lgkmcnt(8)
	global_load_dwordx4 v[76:79], v[80:81], off
	global_load_dwordx4 v[84:87], v[80:81], off offset:16
	s_waitcnt vmcnt(3) lgkmcnt(1)
	v_pk_mul_f32 v[52:53], v[52:53], v[72:73]
	v_pk_mul_f32 v[50:51], v[50:51], v[70:71]
	s_waitcnt vmcnt(2) lgkmcnt(0)
	v_pk_mul_f32 v[56:57], v[56:57], v[68:69]
	v_pk_mul_f32 v[54:55], v[54:55], v[66:67]
	v_xor_b32_e32 v66, 0x80000000, v52
	v_xor_b32_e32 v67, 0x80000000, v53
	v_xor_b32_e32 v68, 0x80000000, v50
	v_xor_b32_e32 v69, 0x80000000, v51
	v_xor_b32_e32 v70, 0x80000000, v56
	v_xor_b32_e32 v71, 0x80000000, v57
	v_xor_b32_e32 v72, 0x80000000, v54
	v_xor_b32_e32 v73, 0x80000000, v55
	v_cndmask_b32_e64 v53, v53, v67, s[8:9]
	v_cndmask_b32_e64 v52, v52, v66, s[8:9]
	v_cndmask_b32_e64 v51, v51, v69, s[8:9]
	v_cndmask_b32_e64 v50, v50, v68, s[8:9]
	v_cndmask_b32_e64 v57, v57, v71, s[8:9]
	v_cndmask_b32_e64 v56, v56, v70, s[8:9]
	v_cndmask_b32_e64 v55, v55, v73, s[8:9]
	v_cndmask_b32_e64 v54, v54, v72, s[8:9]
	s_waitcnt vmcnt(1)
	v_pk_fma_f32 v[48:49], v[48:49], v[78:79], v[52:53]
	v_pk_fma_f32 v[46:47], v[46:47], v[76:77], v[50:51]
	s_waitcnt vmcnt(0)
	v_pk_fma_f32 v[44:45], v[44:45], v[86:87], v[56:57]
	v_pk_fma_f32 v[42:43], v[42:43], v[84:85], v[54:55]
.LBB0_215:
	s_or_b64 exec, exec, s[50:51]
	v_pk_mul_f32 v[40:41], v[40:41], v[64:65]
	v_pk_mul_f32 v[38:39], v[38:39], v[62:63]
	v_pk_mul_f32 v[36:37], v[36:37], v[60:61]
	v_pk_mul_f32 v[34:35], v[34:35], v[58:59]
	s_mov_b32 s100, -1
	s_mov_b32 s101, 0
	v_mov_b32_e32 v244, v38
	v_mov_b32_e32 v54, v38
	s_nop 1
	v_permlane32_swap_b32_e32 v244, v54
	v_cndmask_b32_e64 v54, v244, v54, s[100:101]
	s_mov_b32 s100, -1
	s_mov_b32 s101, 0
	v_mov_b32_e32 v244, v34
	v_mov_b32_e32 v50, v34
	s_nop 1
	v_permlane32_swap_b32_e32 v244, v50
	v_cndmask_b32_e64 v50, v244, v50, s[100:101]
	s_mov_b32 s100, -1
	s_mov_b32 s101, 0
	v_mov_b32_e32 v244, v39
	v_mov_b32_e32 v55, v39
	s_nop 1
	v_permlane32_swap_b32_e32 v244, v55
	v_cndmask_b32_e64 v55, v244, v55, s[100:101]
	s_mov_b32 s100, -1
	s_mov_b32 s101, 0
	v_mov_b32_e32 v244, v35
	v_mov_b32_e32 v51, v35
	s_nop 1
	v_permlane32_swap_b32_e32 v244, v51
	v_cndmask_b32_e64 v51, v244, v51, s[100:101]
	s_mov_b32 s100, -1
	s_mov_b32 s101, 0
	v_mov_b32_e32 v244, v40
	v_mov_b32_e32 v56, v40
	s_nop 1
	v_permlane32_swap_b32_e32 v244, v56
	v_cndmask_b32_e64 v56, v244, v56, s[100:101]
	s_mov_b32 s100, -1
	s_mov_b32 s101, 0
	v_mov_b32_e32 v244, v36
	v_mov_b32_e32 v52, v36
	s_nop 1
	v_permlane32_swap_b32_e32 v244, v52
	v_cndmask_b32_e64 v52, v244, v52, s[100:101]
	s_mov_b32 s100, -1
	s_mov_b32 s101, 0
	v_mov_b32_e32 v244, v41
	v_mov_b32_e32 v57, v41
	s_nop 1
	v_permlane32_swap_b32_e32 v244, v57
	v_cndmask_b32_e64 v57, v244, v57, s[100:101]
	s_mov_b32 s100, -1
	s_mov_b32 s101, 0
	v_mov_b32_e32 v244, v37
	v_mov_b32_e32 v53, v37
	s_nop 1
	v_permlane32_swap_b32_e32 v244, v53
	v_cndmask_b32_e64 v53, v244, v53, s[100:101]
	s_waitcnt lgkmcnt(12)
	v_lshlrev_b64 v[66:67], 8, v[114:115]
	v_lshl_add_u64 v[66:67], v[142:143], 0, v[66:67]
	v_cmp_gt_i32_e32 vcc, s64, v106
	global_store_dwordx4 v[66:67], v[46:49], off
	global_store_dwordx4 v[66:67], v[42:45], off offset:16
	s_and_saveexec_b64 s[50:51], vcc
	s_cbranch_execz .LBB0_217
	v_mov_b32_e32 v42, s26
	v_cndmask_b32_e64 v42, v164, v42, s[10:11]
	v_lshlrev_b32_e32 v138, 6, v42
	v_lshl_add_u64 v[46:47], v[146:147], 0, v[138:139]
	global_load_dwordx4 v[42:45], v[46:47], off
	s_nop 0
	global_load_dwordx4 v[46:49], v[46:47], off offset:16
	v_lshl_add_u64 v[70:71], v[140:141], 0, v[138:139]
	s_waitcnt lgkmcnt(8)
	global_load_dwordx4 v[66:69], v[70:71], off
	s_nop 0
	global_load_dwordx4 v[70:73], v[70:71], off offset:16
	s_waitcnt vmcnt(3) lgkmcnt(1)
	v_pk_mul_f32 v[44:45], v[44:45], v[56:57]
	v_pk_mul_f32 v[42:43], v[42:43], v[54:55]
	s_waitcnt vmcnt(2) lgkmcnt(0)
	v_pk_mul_f32 v[48:49], v[48:49], v[52:53]
	v_pk_mul_f32 v[46:47], v[46:47], v[50:51]
	v_xor_b32_e32 v50, 0x80000000, v44
	v_xor_b32_e32 v51, 0x80000000, v45
	v_xor_b32_e32 v52, 0x80000000, v42
	v_xor_b32_e32 v53, 0x80000000, v43
	v_xor_b32_e32 v54, 0x80000000, v48
	v_xor_b32_e32 v55, 0x80000000, v49
	v_xor_b32_e32 v56, 0x80000000, v46
	v_xor_b32_e32 v57, 0x80000000, v47
	v_cndmask_b32_e64 v45, v45, v51, s[8:9]
	v_cndmask_b32_e64 v44, v44, v50, s[8:9]
	v_cndmask_b32_e64 v43, v43, v53, s[8:9]
	v_cndmask_b32_e64 v42, v42, v52, s[8:9]
	v_cndmask_b32_e64 v49, v49, v55, s[8:9]
	v_cndmask_b32_e64 v48, v48, v54, s[8:9]
	v_cndmask_b32_e64 v47, v47, v57, s[8:9]
	v_cndmask_b32_e64 v46, v46, v56, s[8:9]
	s_waitcnt vmcnt(1)
	v_pk_fma_f32 v[40:41], v[40:41], v[68:69], v[44:45]
	v_pk_fma_f32 v[38:39], v[38:39], v[66:67], v[42:43]
	s_waitcnt vmcnt(0)
	v_pk_fma_f32 v[36:37], v[36:37], v[72:73], v[48:49]
	v_pk_fma_f32 v[34:35], v[34:35], v[70:71], v[46:47]
.LBB0_217:
	s_or_b64 exec, exec, s[50:51]
	v_lshlrev_b64 v[42:43], 8, v[106:107]
	v_pk_mul_f32 v[32:33], v[32:33], v[64:65]
	v_pk_mul_f32 v[30:31], v[30:31], v[62:63]
	v_pk_mul_f32 v[28:29], v[28:29], v[60:61]
	v_pk_mul_f32 v[26:27], v[26:27], v[58:59]
	s_waitcnt lgkmcnt(4)
	v_lshl_add_u64 v[50:51], v[142:143], 0, v[42:43]
	s_mov_b32 s100, -1
	s_mov_b32 s101, 0
	v_mov_b32_e32 v244, v30
	v_mov_b32_e32 v46, v30
	s_nop 1
	v_permlane32_swap_b32_e32 v244, v46
	v_cndmask_b32_e64 v46, v244, v46, s[100:101]
	s_mov_b32 s100, -1
	s_mov_b32 s101, 0
	v_mov_b32_e32 v244, v26
	v_mov_b32_e32 v42, v26
	s_nop 1
	v_permlane32_swap_b32_e32 v244, v42
	v_cndmask_b32_e64 v42, v244, v42, s[100:101]
	s_mov_b32 s100, -1
	s_mov_b32 s101, 0
	v_mov_b32_e32 v244, v31
	v_mov_b32_e32 v47, v31
	s_nop 1
	v_permlane32_swap_b32_e32 v244, v47
	v_cndmask_b32_e64 v47, v244, v47, s[100:101]
	s_mov_b32 s100, -1
	s_mov_b32 s101, 0
	v_mov_b32_e32 v244, v27
	v_mov_b32_e32 v43, v27
	s_nop 1
	v_permlane32_swap_b32_e32 v244, v43
	v_cndmask_b32_e64 v43, v244, v43, s[100:101]
	s_mov_b32 s100, -1
	s_mov_b32 s101, 0
	v_mov_b32_e32 v244, v32
	v_mov_b32_e32 v48, v32
	s_nop 1
	v_permlane32_swap_b32_e32 v244, v48
	v_cndmask_b32_e64 v48, v244, v48, s[100:101]
	s_mov_b32 s100, -1
	s_mov_b32 s101, 0
	v_mov_b32_e32 v244, v28
	v_mov_b32_e32 v44, v28
	s_nop 1
	v_permlane32_swap_b32_e32 v244, v44
	v_cndmask_b32_e64 v44, v244, v44, s[100:101]
	s_mov_b32 s100, -1
	s_mov_b32 s101, 0
	v_mov_b32_e32 v244, v33
	v_mov_b32_e32 v49, v33
	s_nop 1
	v_permlane32_swap_b32_e32 v244, v49
	v_cndmask_b32_e64 v49, v244, v49, s[100:101]
	s_mov_b32 s100, -1
	s_mov_b32 s101, 0
	v_mov_b32_e32 v244, v29
	v_mov_b32_e32 v45, v29
	s_nop 1
	v_permlane32_swap_b32_e32 v244, v45
	v_cndmask_b32_e64 v45, v244, v45, s[100:101]
	global_store_dwordx4 v[50:51], v[38:41], off
	global_store_dwordx4 v[50:51], v[34:37], off offset:16
	v_bfe_u32 v50, v98, 6, 8
	v_cmp_gt_i32_e32 vcc, s75, v156
	s_and_saveexec_b64 s[50:51], vcc
	s_cbranch_execz .LBB0_219
	v_cndmask_b32_e64 v34, v1, v50, s[10:11]
	v_lshlrev_b32_e32 v138, 6, v34
	v_lshl_add_u64 v[38:39], v[146:147], 0, v[138:139]
	global_load_dwordx4 v[34:37], v[38:39], off
	s_nop 0
	global_load_dwordx4 v[38:41], v[38:39], off offset:16
	s_waitcnt lgkmcnt(9)
	v_lshl_add_u64 v[56:57], v[140:141], 0, v[138:139]
	s_waitcnt lgkmcnt(8)
	global_load_dwordx4 v[52:55], v[56:57], off
	global_load_dwordx4 v[66:69], v[56:57], off offset:16
	s_waitcnt vmcnt(3) lgkmcnt(1)
	v_pk_mul_f32 v[36:37], v[36:37], v[48:49]
	v_pk_mul_f32 v[34:35], v[34:35], v[46:47]
	s_waitcnt vmcnt(2) lgkmcnt(0)
	v_pk_mul_f32 v[40:41], v[40:41], v[44:45]
	v_pk_mul_f32 v[38:39], v[38:39], v[42:43]
	v_xor_b32_e32 v42, 0x80000000, v36
	v_xor_b32_e32 v43, 0x80000000, v37
	v_xor_b32_e32 v44, 0x80000000, v34
	v_xor_b32_e32 v45, 0x80000000, v35
	v_xor_b32_e32 v46, 0x80000000, v40
	v_xor_b32_e32 v47, 0x80000000, v41
	v_xor_b32_e32 v48, 0x80000000, v38
	v_xor_b32_e32 v49, 0x80000000, v39
	v_cndmask_b32_e64 v37, v37, v43, s[8:9]
	v_cndmask_b32_e64 v36, v36, v42, s[8:9]
	v_cndmask_b32_e64 v35, v35, v45, s[8:9]
	v_cndmask_b32_e64 v34, v34, v44, s[8:9]
	v_cndmask_b32_e64 v41, v41, v47, s[8:9]
	v_cndmask_b32_e64 v40, v40, v46, s[8:9]
	v_cndmask_b32_e64 v39, v39, v49, s[8:9]
	v_cndmask_b32_e64 v38, v38, v48, s[8:9]
	s_waitcnt vmcnt(1)
	v_pk_fma_f32 v[32:33], v[32:33], v[54:55], v[36:37]
	v_pk_fma_f32 v[30:31], v[30:31], v[52:53], v[34:35]
	s_waitcnt vmcnt(0)
	v_pk_fma_f32 v[28:29], v[28:29], v[68:69], v[40:41]
	v_pk_fma_f32 v[26:27], v[26:27], v[66:67], v[38:39]
.LBB0_219:
	s_or_b64 exec, exec, s[50:51]
	v_pk_mul_f32 v[24:25], v[24:25], v[64:65]
	v_pk_mul_f32 v[22:23], v[22:23], v[62:63]
	v_pk_mul_f32 v[20:21], v[20:21], v[60:61]
	v_pk_mul_f32 v[18:19], v[18:19], v[58:59]
	s_mov_b32 s100, -1
	s_mov_b32 s101, 0
	v_mov_b32_e32 v244, v22
	v_mov_b32_e32 v38, v22
	s_nop 1
	v_permlane32_swap_b32_e32 v244, v38
	v_cndmask_b32_e64 v38, v244, v38, s[100:101]
	s_mov_b32 s100, -1
	s_mov_b32 s101, 0
	v_mov_b32_e32 v244, v18
	v_mov_b32_e32 v34, v18
	s_nop 1
	v_permlane32_swap_b32_e32 v244, v34
	v_cndmask_b32_e64 v34, v244, v34, s[100:101]
	s_mov_b32 s100, -1
	s_mov_b32 s101, 0
	v_mov_b32_e32 v244, v23
	v_mov_b32_e32 v39, v23
	s_nop 1
	v_permlane32_swap_b32_e32 v244, v39
	v_cndmask_b32_e64 v39, v244, v39, s[100:101]
	s_mov_b32 s100, -1
	s_mov_b32 s101, 0
	v_mov_b32_e32 v244, v19
	v_mov_b32_e32 v35, v19
	s_nop 1
	v_permlane32_swap_b32_e32 v244, v35
	v_cndmask_b32_e64 v35, v244, v35, s[100:101]
	s_mov_b32 s100, -1
	s_mov_b32 s101, 0
	v_mov_b32_e32 v244, v24
	v_mov_b32_e32 v40, v24
	s_nop 1
	v_permlane32_swap_b32_e32 v244, v40
	v_cndmask_b32_e64 v40, v244, v40, s[100:101]
	s_mov_b32 s100, -1
	s_mov_b32 s101, 0
	v_mov_b32_e32 v244, v20
	v_mov_b32_e32 v36, v20
	s_nop 1
	v_permlane32_swap_b32_e32 v244, v36
	v_cndmask_b32_e64 v36, v244, v36, s[100:101]
	s_mov_b32 s100, -1
	s_mov_b32 s101, 0
	v_mov_b32_e32 v244, v25
	v_mov_b32_e32 v41, v25
	s_nop 1
	v_permlane32_swap_b32_e32 v244, v41
	v_cndmask_b32_e64 v41, v244, v41, s[100:101]
	s_mov_b32 s100, -1
	s_mov_b32 s101, 0
	v_mov_b32_e32 v244, v21
	v_mov_b32_e32 v37, v21
	s_nop 1
	v_permlane32_swap_b32_e32 v244, v37
	v_cndmask_b32_e64 v37, v244, v37, s[100:101]
	s_waitcnt lgkmcnt(12)
	v_lshlrev_b64 v[42:43], 8, v[98:99]
	v_lshl_add_u64 v[42:43], v[142:143], 0, v[42:43]
	v_cmp_gt_i32_e32 vcc, s76, v156
	global_store_dwordx4 v[42:43], v[30:33], off
	global_store_dwordx4 v[42:43], v[26:29], off offset:16
	s_and_saveexec_b64 s[50:51], vcc
	s_cbranch_execz .LBB0_221
	v_cndmask_b32_e64 v26, v162, v50, s[10:11]
	v_lshlrev_b32_e32 v138, 6, v26
	v_lshl_add_u64 v[30:31], v[146:147], 0, v[138:139]
	global_load_dwordx4 v[26:29], v[30:31], off
	s_nop 0
	global_load_dwordx4 v[30:33], v[30:31], off offset:16
	v_lshl_add_u64 v[46:47], v[140:141], 0, v[138:139]
	s_waitcnt lgkmcnt(8)
	global_load_dwordx4 v[42:45], v[46:47], off
	s_nop 0
	global_load_dwordx4 v[46:49], v[46:47], off offset:16
	s_waitcnt vmcnt(3) lgkmcnt(1)
	v_pk_mul_f32 v[28:29], v[28:29], v[40:41]
	v_pk_mul_f32 v[26:27], v[26:27], v[38:39]
	s_waitcnt vmcnt(2) lgkmcnt(0)
	v_pk_mul_f32 v[32:33], v[32:33], v[36:37]
	v_pk_mul_f32 v[30:31], v[30:31], v[34:35]
	v_xor_b32_e32 v34, 0x80000000, v28
	v_xor_b32_e32 v35, 0x80000000, v29
	v_xor_b32_e32 v36, 0x80000000, v26
	v_xor_b32_e32 v37, 0x80000000, v27
	v_xor_b32_e32 v38, 0x80000000, v32
	v_xor_b32_e32 v39, 0x80000000, v33
	v_xor_b32_e32 v40, 0x80000000, v30
	v_xor_b32_e32 v41, 0x80000000, v31
	v_cndmask_b32_e64 v29, v29, v35, s[8:9]
	v_cndmask_b32_e64 v28, v28, v34, s[8:9]
	v_cndmask_b32_e64 v27, v27, v37, s[8:9]
	v_cndmask_b32_e64 v26, v26, v36, s[8:9]
	v_cndmask_b32_e64 v33, v33, v39, s[8:9]
	v_cndmask_b32_e64 v32, v32, v38, s[8:9]
	v_cndmask_b32_e64 v31, v31, v41, s[8:9]
	v_cndmask_b32_e64 v30, v30, v40, s[8:9]
	s_waitcnt vmcnt(1)
	v_pk_fma_f32 v[24:25], v[24:25], v[44:45], v[28:29]
	v_pk_fma_f32 v[22:23], v[22:23], v[42:43], v[26:27]
	s_waitcnt vmcnt(0)
	v_pk_fma_f32 v[20:21], v[20:21], v[48:49], v[32:33]
	v_pk_fma_f32 v[18:19], v[18:19], v[46:47], v[30:31]
.LBB0_221:
	s_or_b64 exec, exec, s[50:51]
	v_pk_mul_f32 v[16:17], v[16:17], v[64:65]
	v_pk_mul_f32 v[14:15], v[14:15], v[62:63]
	v_pk_mul_f32 v[12:13], v[12:13], v[60:61]
	v_pk_mul_f32 v[10:11], v[10:11], v[58:59]
	s_mov_b32 s100, -1
	s_mov_b32 s101, 0
	v_mov_b32_e32 v244, v14
	v_mov_b32_e32 v30, v14
	s_nop 1
	v_permlane32_swap_b32_e32 v244, v30
	v_cndmask_b32_e64 v30, v244, v30, s[100:101]
	s_mov_b32 s100, -1
	s_mov_b32 s101, 0
	v_mov_b32_e32 v244, v10
	v_mov_b32_e32 v26, v10
	s_nop 1
	v_permlane32_swap_b32_e32 v244, v26
	v_cndmask_b32_e64 v26, v244, v26, s[100:101]
	s_mov_b32 s100, -1
	s_mov_b32 s101, 0
	v_mov_b32_e32 v244, v15
	v_mov_b32_e32 v31, v15
	s_nop 1
	v_permlane32_swap_b32_e32 v244, v31
	v_cndmask_b32_e64 v31, v244, v31, s[100:101]
	s_mov_b32 s100, -1
	s_mov_b32 s101, 0
	v_mov_b32_e32 v244, v11
	v_mov_b32_e32 v27, v11
	s_nop 1
	v_permlane32_swap_b32_e32 v244, v27
	v_cndmask_b32_e64 v27, v244, v27, s[100:101]
	s_mov_b32 s100, -1
	s_mov_b32 s101, 0
	v_mov_b32_e32 v244, v16
	v_mov_b32_e32 v32, v16
	s_nop 1
	v_permlane32_swap_b32_e32 v244, v32
	v_cndmask_b32_e64 v32, v244, v32, s[100:101]
	s_mov_b32 s100, -1
	s_mov_b32 s101, 0
	v_mov_b32_e32 v244, v12
	v_mov_b32_e32 v28, v12
	s_nop 1
	v_permlane32_swap_b32_e32 v244, v28
	v_cndmask_b32_e64 v28, v244, v28, s[100:101]
	s_mov_b32 s100, -1
	s_mov_b32 s101, 0
	v_mov_b32_e32 v244, v17
	v_mov_b32_e32 v33, v17
	s_nop 1
	v_permlane32_swap_b32_e32 v244, v33
	v_cndmask_b32_e64 v33, v244, v33, s[100:101]
	s_mov_b32 s100, -1
	s_mov_b32 s101, 0
	v_mov_b32_e32 v244, v13
	v_mov_b32_e32 v29, v13
	s_nop 1
	v_permlane32_swap_b32_e32 v244, v29
	v_cndmask_b32_e64 v29, v244, v29, s[100:101]
	s_waitcnt lgkmcnt(12)
	v_lshlrev_b64 v[34:35], 8, v[90:91]
	v_lshl_add_u64 v[34:35], v[142:143], 0, v[34:35]
	v_cmp_gt_i32_e32 vcc, s77, v156
	global_store_dwordx4 v[34:35], v[22:25], off
	global_store_dwordx4 v[34:35], v[18:21], off offset:16
	s_and_saveexec_b64 s[50:51], vcc
	s_cbranch_execz .LBB0_223
	v_cndmask_b32_e64 v18, v163, v50, s[10:11]
	v_lshlrev_b32_e32 v138, 6, v18
	v_lshl_add_u64 v[22:23], v[146:147], 0, v[138:139]
	global_load_dwordx4 v[18:21], v[22:23], off
	s_nop 0
	global_load_dwordx4 v[22:25], v[22:23], off offset:16
	v_lshl_add_u64 v[38:39], v[140:141], 0, v[138:139]
	s_waitcnt lgkmcnt(8)
	global_load_dwordx4 v[34:37], v[38:39], off
	s_nop 0
	global_load_dwordx4 v[38:41], v[38:39], off offset:16
	s_waitcnt vmcnt(3) lgkmcnt(1)
	v_pk_mul_f32 v[20:21], v[20:21], v[32:33]
	v_pk_mul_f32 v[18:19], v[18:19], v[30:31]
	s_waitcnt vmcnt(2) lgkmcnt(0)
	v_pk_mul_f32 v[24:25], v[24:25], v[28:29]
	v_pk_mul_f32 v[22:23], v[22:23], v[26:27]
	v_xor_b32_e32 v26, 0x80000000, v20
	v_xor_b32_e32 v27, 0x80000000, v21
	v_xor_b32_e32 v28, 0x80000000, v18
	v_xor_b32_e32 v29, 0x80000000, v19
	v_xor_b32_e32 v30, 0x80000000, v24
	v_xor_b32_e32 v31, 0x80000000, v25
	v_xor_b32_e32 v32, 0x80000000, v22
	v_xor_b32_e32 v33, 0x80000000, v23
	v_cndmask_b32_e64 v21, v21, v27, s[8:9]
	v_cndmask_b32_e64 v20, v20, v26, s[8:9]
	v_cndmask_b32_e64 v19, v19, v29, s[8:9]
	v_cndmask_b32_e64 v18, v18, v28, s[8:9]
	v_cndmask_b32_e64 v25, v25, v31, s[8:9]
	v_cndmask_b32_e64 v24, v24, v30, s[8:9]
	v_cndmask_b32_e64 v23, v23, v33, s[8:9]
	v_cndmask_b32_e64 v22, v22, v32, s[8:9]
	s_waitcnt vmcnt(1)
	v_pk_fma_f32 v[16:17], v[16:17], v[36:37], v[20:21]
	v_pk_fma_f32 v[14:15], v[14:15], v[34:35], v[18:19]
	s_waitcnt vmcnt(0)
	v_pk_fma_f32 v[12:13], v[12:13], v[40:41], v[24:25]
	v_pk_fma_f32 v[10:11], v[10:11], v[38:39], v[22:23]
.LBB0_223:
	s_or_b64 exec, exec, s[50:51]
	v_pk_mul_f32 v[8:9], v[8:9], v[64:65]
	v_pk_mul_f32 v[6:7], v[6:7], v[62:63]
	v_pk_mul_f32 v[4:5], v[4:5], v[60:61]
	v_pk_mul_f32 v[2:3], v[2:3], v[58:59]
	s_mov_b32 s100, -1
	s_mov_b32 s101, 0
	v_mov_b32_e32 v244, v6
	v_mov_b32_e32 v22, v6
	s_nop 1
	v_permlane32_swap_b32_e32 v244, v22
	v_cndmask_b32_e64 v22, v244, v22, s[100:101]
	s_mov_b32 s100, -1
	s_mov_b32 s101, 0
	v_mov_b32_e32 v244, v2
	v_mov_b32_e32 v18, v2
	s_nop 1
	v_permlane32_swap_b32_e32 v244, v18
	v_cndmask_b32_e64 v18, v244, v18, s[100:101]
	s_mov_b32 s100, -1
	s_mov_b32 s101, 0
	v_mov_b32_e32 v244, v7
	v_mov_b32_e32 v23, v7
	s_nop 1
	v_permlane32_swap_b32_e32 v244, v23
	v_cndmask_b32_e64 v23, v244, v23, s[100:101]
	s_mov_b32 s100, -1
	s_mov_b32 s101, 0
	v_mov_b32_e32 v244, v3
	v_mov_b32_e32 v19, v3
	s_nop 1
	v_permlane32_swap_b32_e32 v244, v19
	v_cndmask_b32_e64 v19, v244, v19, s[100:101]
	s_mov_b32 s100, -1
	s_mov_b32 s101, 0
	v_mov_b32_e32 v244, v8
	v_mov_b32_e32 v24, v8
	s_nop 1
	v_permlane32_swap_b32_e32 v244, v24
	v_cndmask_b32_e64 v24, v244, v24, s[100:101]
	s_mov_b32 s100, -1
	s_mov_b32 s101, 0
	v_mov_b32_e32 v244, v4
	v_mov_b32_e32 v20, v4
	s_nop 1
	v_permlane32_swap_b32_e32 v244, v20
	v_cndmask_b32_e64 v20, v244, v20, s[100:101]
	s_mov_b32 s100, -1
	s_mov_b32 s101, 0
	v_mov_b32_e32 v244, v9
	v_mov_b32_e32 v25, v9
	s_nop 1
	v_permlane32_swap_b32_e32 v244, v25
	v_cndmask_b32_e64 v25, v244, v25, s[100:101]
	s_mov_b32 s100, -1
	s_mov_b32 s101, 0
	v_mov_b32_e32 v244, v5
	v_mov_b32_e32 v21, v5
	s_nop 1
	v_permlane32_swap_b32_e32 v244, v21
	v_cndmask_b32_e64 v21, v244, v21, s[100:101]
	s_waitcnt lgkmcnt(12)
	v_lshlrev_b64 v[26:27], 8, v[82:83]
	v_lshl_add_u64 v[26:27], v[142:143], 0, v[26:27]
	v_cmp_gt_i32_e32 vcc, s78, v156
	global_store_dwordx4 v[26:27], v[14:17], off
	global_store_dwordx4 v[26:27], v[10:13], off offset:16
	s_and_saveexec_b64 s[50:51], vcc
	s_cbranch_execz .LBB0_225
	v_cndmask_b32_e64 v10, v164, v50, s[10:11]
	v_lshlrev_b32_e32 v138, 6, v10
	v_lshl_add_u64 v[14:15], v[146:147], 0, v[138:139]
	global_load_dwordx4 v[10:13], v[14:15], off
	s_nop 0
	global_load_dwordx4 v[14:17], v[14:15], off offset:16
	v_lshl_add_u64 v[30:31], v[140:141], 0, v[138:139]
	s_waitcnt lgkmcnt(8)
	global_load_dwordx4 v[26:29], v[30:31], off
	s_nop 0
	global_load_dwordx4 v[30:33], v[30:31], off offset:16
	s_waitcnt vmcnt(3) lgkmcnt(1)
	v_pk_mul_f32 v[12:13], v[12:13], v[24:25]
	v_pk_mul_f32 v[10:11], v[10:11], v[22:23]
	s_waitcnt vmcnt(2) lgkmcnt(0)
	v_pk_mul_f32 v[16:17], v[16:17], v[20:21]
	v_pk_mul_f32 v[14:15], v[14:15], v[18:19]
	v_xor_b32_e32 v18, 0x80000000, v12
	v_xor_b32_e32 v19, 0x80000000, v13
	v_xor_b32_e32 v20, 0x80000000, v10
	v_xor_b32_e32 v21, 0x80000000, v11
	v_xor_b32_e32 v22, 0x80000000, v16
	v_xor_b32_e32 v23, 0x80000000, v17
	v_xor_b32_e32 v24, 0x80000000, v14
	v_xor_b32_e32 v25, 0x80000000, v15
	v_cndmask_b32_e64 v13, v13, v19, s[8:9]
	v_cndmask_b32_e64 v12, v12, v18, s[8:9]
	v_cndmask_b32_e64 v11, v11, v21, s[8:9]
	v_cndmask_b32_e64 v10, v10, v20, s[8:9]
	v_cndmask_b32_e64 v17, v17, v23, s[8:9]
	v_cndmask_b32_e64 v16, v16, v22, s[8:9]
	v_cndmask_b32_e64 v15, v15, v25, s[8:9]
	v_cndmask_b32_e64 v14, v14, v24, s[8:9]
	s_waitcnt vmcnt(1)
	v_pk_fma_f32 v[8:9], v[8:9], v[28:29], v[12:13]
	v_pk_fma_f32 v[6:7], v[6:7], v[26:27], v[10:11]
	s_waitcnt vmcnt(0)
	v_pk_fma_f32 v[4:5], v[4:5], v[32:33], v[16:17]
	v_pk_fma_f32 v[2:3], v[2:3], v[30:31], v[14:15]

.LBB0_357:
	global_load_dwordx4 v[90:93], v[152:153], off offset:16
	global_load_dwordx4 v[94:97], v[152:153], off
	v_mul_f32_e32 v166, v135, v135
	v_mul_f32_e32 v167, v137, v137
	v_and_b32_e32 v165, 64, v174
	v_fmac_f32_e32 v166, v134, v134
	v_fmac_f32_e32 v167, v136, v136
	v_xor_b32_e32 v164, 16, v174
	v_add_u32_e32 v165, 64, v165
	v_add_f32_e32 v166, v166, v167
	v_mul_f32_e32 v167, v131, v131
	v_mul_f32_e32 v176, v133, v133
	v_cmp_lt_i32_e32 vcc, v164, v165
	v_fmac_f32_e32 v167, v130, v130
	v_fmac_f32_e32 v176, v132, v132
	v_cndmask_b32_e32 v164, v174, v164, vcc
	v_add_f32_e32 v167, v167, v176
	v_lshlrev_b32_e32 v164, 2, v164
	v_add_f32_e32 v167, v166, v167
	s_mov_b32 s100, 0xffff
	s_mov_b32 s101, 0xffff
	v_mov_b32_e32 v244, v167
	v_mov_b32_e32 v176, v167
	s_nop 1
	v_permlane16_swap_b32_e32 v244, v176
	v_cndmask_b32_e64 v176, v244, v176, s[100:101]
	v_xor_b32_e32 v166, 32, v174
	v_cmp_lt_i32_e32 vcc, v166, v165
	s_waitcnt lgkmcnt(0)
	v_add_f32_e32 v167, v167, v176
	v_cndmask_b32_e32 v165, v174, v166, vcc
	v_lshlrev_b32_e32 v166, 2, v165
	s_mov_b32 s100, -1
	s_mov_b32 s101, 0
	v_mov_b32_e32 v244, v167
	v_mov_b32_e32 v176, v167
	s_nop 1
	v_permlane32_swap_b32_e32 v244, v176
	v_cndmask_b32_e64 v176, v244, v176, s[100:101]
	v_add_u32_e32 v165, s65, v169
	s_and_saveexec_b64 s[10:11], s[6:7]
	s_cbranch_execz .LBB0_359
	s_waitcnt lgkmcnt(0)
	v_add_f32_e32 v167, v167, v176
	ds_write_b32 v165, v167
.LBB0_359:
	s_or_b64 exec, exec, s[10:11]
	v_mul_f32_e32 v167, v127, v127
	s_waitcnt lgkmcnt(0)
	v_mul_f32_e32 v176, v129, v129
	v_fmac_f32_e32 v167, v126, v126
	v_fmac_f32_e32 v176, v128, v128
	v_add_f32_e32 v167, v167, v176
	v_mul_f32_e32 v176, v123, v123
	v_mul_f32_e32 v177, v125, v125
	v_fmac_f32_e32 v176, v122, v122
	v_fmac_f32_e32 v177, v124, v124
	v_add_f32_e32 v176, v176, v177
	v_add_f32_e32 v167, v167, v176
	s_mov_b32 s100, 0xffff
	s_mov_b32 s101, 0xffff
	v_mov_b32_e32 v244, v167
	v_mov_b32_e32 v176, v167
	s_nop 1
	v_permlane16_swap_b32_e32 v244, v176
	v_cndmask_b32_e64 v176, v244, v176, s[100:101]
	s_waitcnt lgkmcnt(0)
	v_add_f32_e32 v167, v167, v176
	s_mov_b32 s100, -1
	s_mov_b32 s101, 0
	v_mov_b32_e32 v244, v167
	v_mov_b32_e32 v176, v167
	s_nop 1
	v_permlane32_swap_b32_e32 v244, v176
	v_cndmask_b32_e64 v176, v244, v176, s[100:101]
	s_and_saveexec_b64 s[10:11], s[6:7]
	s_cbranch_execz .LBB0_361
	s_waitcnt lgkmcnt(0)
	v_add_f32_e32 v167, v167, v176
	ds_write_b32 v165, v167 offset:256
.LBB0_361:
	s_or_b64 exec, exec, s[10:11]
	v_mul_f32_e32 v167, v119, v119
	s_waitcnt lgkmcnt(0)
	v_mul_f32_e32 v176, v121, v121
	v_fmac_f32_e32 v167, v118, v118
	v_fmac_f32_e32 v176, v120, v120
	v_add_f32_e32 v167, v167, v176
	v_mul_f32_e32 v176, v115, v115
	v_mul_f32_e32 v177, v117, v117
	v_fmac_f32_e32 v176, v114, v114
	v_fmac_f32_e32 v177, v116, v116
	v_add_f32_e32 v176, v176, v177
	v_add_f32_e32 v167, v167, v176
	s_mov_b32 s100, 0xffff
	s_mov_b32 s101, 0xffff
	v_mov_b32_e32 v244, v167
	v_mov_b32_e32 v176, v167
	s_nop 1
	v_permlane16_swap_b32_e32 v244, v176
	v_cndmask_b32_e64 v176, v244, v176, s[100:101]
	s_waitcnt lgkmcnt(0)
	v_add_f32_e32 v167, v167, v176
	s_mov_b32 s100, -1
	s_mov_b32 s101, 0
	v_mov_b32_e32 v244, v167
	v_mov_b32_e32 v176, v167
	s_nop 1
	v_permlane32_swap_b32_e32 v244, v176
	v_cndmask_b32_e64 v176, v244, v176, s[100:101]
	s_and_saveexec_b64 s[10:11], s[6:7]
	s_cbranch_execz .LBB0_363
	s_waitcnt lgkmcnt(0)
	v_add_f32_e32 v167, v167, v176
	ds_write_b32 v165, v167 offset:512
.LBB0_363:
	s_or_b64 exec, exec, s[10:11]
	v_mul_f32_e32 v167, v111, v111
	s_waitcnt lgkmcnt(0)
	v_mul_f32_e32 v176, v113, v113
	v_fmac_f32_e32 v167, v110, v110
	v_fmac_f32_e32 v176, v112, v112
	v_add_f32_e32 v167, v167, v176
	v_mul_f32_e32 v176, v107, v107
	v_mul_f32_e32 v177, v109, v109
	v_fmac_f32_e32 v176, v106, v106
	v_fmac_f32_e32 v177, v108, v108
	v_add_f32_e32 v176, v176, v177
	v_add_f32_e32 v167, v167, v176
	s_mov_b32 s100, 0xffff
	s_mov_b32 s101, 0xffff
	v_mov_b32_e32 v244, v167
	v_mov_b32_e32 v176, v167
	s_nop 1
	v_permlane16_swap_b32_e32 v244, v176
	v_cndmask_b32_e64 v176, v244, v176, s[100:101]
	s_waitcnt lgkmcnt(0)
	v_add_f32_e32 v167, v167, v176
	s_mov_b32 s100, -1
	s_mov_b32 s101, 0
	v_mov_b32_e32 v244, v167
	v_mov_b32_e32 v176, v167
	s_nop 1
	v_permlane32_swap_b32_e32 v244, v176
	v_cndmask_b32_e64 v176, v244, v176, s[100:101]
	s_and_saveexec_b64 s[10:11], s[6:7]
	s_cbranch_execz .LBB0_365
	s_waitcnt lgkmcnt(0)
	v_add_f32_e32 v167, v167, v176
	ds_write_b32 v165, v167 offset:768
.LBB0_365:
	s_or_b64 exec, exec, s[10:11]
	v_mul_f32_e32 v167, v103, v103
	s_waitcnt lgkmcnt(0)
	v_mul_f32_e32 v176, v105, v105
	v_fmac_f32_e32 v167, v102, v102
	v_fmac_f32_e32 v176, v104, v104
	v_add_f32_e32 v167, v167, v176
	v_mul_f32_e32 v176, v99, v99
	v_mul_f32_e32 v177, v101, v101
	v_fmac_f32_e32 v176, v98, v98
	v_fmac_f32_e32 v177, v100, v100
	v_add_f32_e32 v176, v176, v177
	v_add_f32_e32 v167, v167, v176
	s_mov_b32 s100, 0xffff
	s_mov_b32 s101, 0xffff
	v_mov_b32_e32 v244, v167
	v_mov_b32_e32 v176, v167
	s_nop 1
	v_permlane16_swap_b32_e32 v244, v176
	v_cndmask_b32_e64 v176, v244, v176, s[100:101]
	s_waitcnt lgkmcnt(0)
	v_add_f32_e32 v167, v167, v176
	s_mov_b32 s100, -1
	s_mov_b32 s101, 0
	v_mov_b32_e32 v244, v167
	v_mov_b32_e32 v176, v167
	s_nop 1
	v_permlane32_swap_b32_e32 v244, v176
	v_cndmask_b32_e64 v176, v244, v176, s[100:101]
	s_and_saveexec_b64 s[10:11], s[6:7]
	s_cbranch_execz .LBB0_367
	s_waitcnt lgkmcnt(0)
	v_add_f32_e32 v167, v167, v176
	ds_write_b32 v165, v167 offset:2048
.LBB0_367:
	s_or_b64 exec, exec, s[10:11]
	v_mul_f32_e32 v167, v87, v87
	s_waitcnt lgkmcnt(0)
	v_mul_f32_e32 v176, v89, v89
	v_fmac_f32_e32 v167, v86, v86
	v_fmac_f32_e32 v176, v88, v88
	v_add_f32_e32 v167, v167, v176
	v_mul_f32_e32 v176, v83, v83
	v_mul_f32_e32 v177, v85, v85
	v_fmac_f32_e32 v176, v82, v82
	v_fmac_f32_e32 v177, v84, v84
	v_add_f32_e32 v176, v176, v177
	v_add_f32_e32 v167, v167, v176
	s_mov_b32 s100, 0xffff
	s_mov_b32 s101, 0xffff
	v_mov_b32_e32 v244, v167
	v_mov_b32_e32 v176, v167
	s_nop 1
	v_permlane16_swap_b32_e32 v244, v176
	v_cndmask_b32_e64 v176, v244, v176, s[100:101]
	s_waitcnt lgkmcnt(0)
	v_add_f32_e32 v167, v167, v176
	s_mov_b32 s100, -1
	s_mov_b32 s101, 0
	v_mov_b32_e32 v244, v167
	v_mov_b32_e32 v176, v167
	s_nop 1
	v_permlane32_swap_b32_e32 v244, v176
	v_cndmask_b32_e64 v176, v244, v176, s[100:101]
	s_and_saveexec_b64 s[10:11], s[6:7]
	s_cbranch_execz .LBB0_369
	s_waitcnt lgkmcnt(0)
	v_add_f32_e32 v167, v167, v176
	ds_write_b32 v165, v167 offset:2304
.LBB0_369:
	s_or_b64 exec, exec, s[10:11]
	v_mul_f32_e32 v167, v79, v79
	s_waitcnt lgkmcnt(0)
	v_mul_f32_e32 v176, v81, v81
	v_fmac_f32_e32 v167, v78, v78
	v_fmac_f32_e32 v176, v80, v80
	v_add_f32_e32 v167, v167, v176
	v_mul_f32_e32 v176, v75, v75
	v_mul_f32_e32 v177, v77, v77
	v_fmac_f32_e32 v176, v74, v74
	v_fmac_f32_e32 v177, v76, v76
	v_add_f32_e32 v176, v176, v177
	v_add_f32_e32 v167, v167, v176
	s_mov_b32 s100, 0xffff
	s_mov_b32 s101, 0xffff
	v_mov_b32_e32 v244, v167
	v_mov_b32_e32 v176, v167
	s_nop 1
	v_permlane16_swap_b32_e32 v244, v176
	v_cndmask_b32_e64 v176, v244, v176, s[100:101]
	s_waitcnt lgkmcnt(0)
	v_add_f32_e32 v167, v167, v176
	s_mov_b32 s100, -1
	s_mov_b32 s101, 0
	v_mov_b32_e32 v244, v167
	v_mov_b32_e32 v176, v167
	s_nop 1
	v_permlane32_swap_b32_e32 v244, v176
	v_cndmask_b32_e64 v176, v244, v176, s[100:101]
	s_and_saveexec_b64 s[10:11], s[6:7]
	s_cbranch_execz .LBB0_371
	s_waitcnt lgkmcnt(0)
	v_add_f32_e32 v167, v167, v176
	ds_write_b32 v165, v167 offset:2560
.LBB0_371:
	s_or_b64 exec, exec, s[10:11]
	v_mul_f32_e32 v167, v27, v27
	s_waitcnt lgkmcnt(0)
	v_mul_f32_e32 v176, v29, v29
	v_fmac_f32_e32 v167, v26, v26
	v_fmac_f32_e32 v176, v28, v28
	v_add_f32_e32 v167, v167, v176
	v_mul_f32_e32 v176, v23, v23
	v_mul_f32_e32 v177, v25, v25
	v_fmac_f32_e32 v176, v22, v22
	v_fmac_f32_e32 v177, v24, v24
	v_add_f32_e32 v176, v176, v177
	v_add_f32_e32 v167, v167, v176
	s_mov_b32 s100, 0xffff
	s_mov_b32 s101, 0xffff
	v_mov_b32_e32 v244, v167
	v_mov_b32_e32 v164, v167
	s_nop 1
	v_permlane16_swap_b32_e32 v244, v164
	v_cndmask_b32_e64 v164, v244, v164, s[100:101]
	s_waitcnt lgkmcnt(0)
	v_add_f32_e32 v164, v167, v164
	s_mov_b32 s100, -1
	s_mov_b32 s101, 0
	v_mov_b32_e32 v244, v164
	v_mov_b32_e32 v166, v164
	s_nop 1
	v_permlane32_swap_b32_e32 v244, v166
	v_cndmask_b32_e64 v166, v244, v166, s[100:101]
	s_and_saveexec_b64 s[10:11], s[6:7]
	s_cbranch_execz .LBB0_373
	s_waitcnt lgkmcnt(0)
	v_add_f32_e32 v164, v164, v166
	ds_write_b32 v165, v164 offset:2816

.LBB0_1415:
	s_cmp_gt_i32 s30, 15
	s_cbranch_scc1 .LBB0_1449
	s_cmp_lt_i32 s30, 8
	s_cselect_b32 s43, s14, s24
	s_cselect_b32 s41, s15, s25
	s_add_u32 s48, s43, s68
	s_addc_u32 s49, s41, 0
	global_load_dwordx4 v[130:133], v160, s[48:49] offset:16
	global_load_dwordx4 v[134:137], v160, s[48:49]
	v_mul_f32_e32 v165, v127, v127
	v_mul_f32_e32 v166, v129, v129
	v_and_b32_e32 v164, 64, v162
	v_fmac_f32_e32 v165, v126, v126
	v_fmac_f32_e32 v166, v128, v128
	v_xor_b32_e32 v163, 16, v162
	v_add_u32_e32 v164, 64, v164
	v_add_f32_e32 v165, v165, v166
	v_mul_f32_e32 v166, v123, v123
	v_mul_f32_e32 v167, v125, v125
	v_cmp_lt_i32_e32 vcc, v163, v164
	v_fmac_f32_e32 v166, v122, v122
	v_fmac_f32_e32 v167, v124, v124
	v_cndmask_b32_e32 v163, v162, v163, vcc
	v_add_f32_e32 v166, v166, v167
	v_lshlrev_b32_e32 v163, 2, v163
	v_add_f32_e32 v165, v165, v166
	s_mov_b32 s100, 0xffff
	s_mov_b32 s101, 0xffff
	v_mov_b32_e32 v244, v165
	v_mov_b32_e32 v166, v165
	s_nop 1
	v_permlane16_swap_b32_e32 v244, v166
	v_cndmask_b32_e64 v166, v244, v166, s[100:101]
	v_xor_b32_e32 v167, 32, v162
	v_cmp_lt_i32_e32 vcc, v167, v164
	s_waitcnt lgkmcnt(0)
	v_add_f32_e32 v166, v165, v166
	v_cndmask_b32_e32 v164, v162, v167, vcc
	v_lshlrev_b32_e32 v164, 2, v164
	s_mov_b32 s100, -1
	s_mov_b32 s101, 0
	v_mov_b32_e32 v244, v166
	v_mov_b32_e32 v167, v166
	s_nop 1
	v_permlane32_swap_b32_e32 v244, v167
	v_cndmask_b32_e64 v167, v244, v167, s[100:101]
	v_add_u32_e32 v165, s61, v155
	s_and_saveexec_b64 s[48:49], s[6:7]
	s_cbranch_execz .LBB0_1418
	s_waitcnt lgkmcnt(0)
	v_add_f32_e32 v166, v166, v167
	ds_write_b32 v165, v166
.LBB0_1418:
	s_or_b64 exec, exec, s[48:49]
	v_mul_f32_e32 v166, v119, v119
	s_waitcnt lgkmcnt(0)
	v_mul_f32_e32 v167, v121, v121
	v_fmac_f32_e32 v166, v118, v118
	v_fmac_f32_e32 v167, v120, v120
	v_add_f32_e32 v166, v166, v167
	v_mul_f32_e32 v167, v115, v115
	v_mul_f32_e32 v168, v117, v117
	v_fmac_f32_e32 v167, v114, v114
	v_fmac_f32_e32 v168, v116, v116
	v_add_f32_e32 v167, v167, v168
	v_add_f32_e32 v166, v166, v167
	s_mov_b32 s100, 0xffff
	s_mov_b32 s101, 0xffff
	v_mov_b32_e32 v244, v166
	v_mov_b32_e32 v167, v166
	s_nop 1
	v_permlane16_swap_b32_e32 v244, v167
	v_cndmask_b32_e64 v167, v244, v167, s[100:101]
	s_waitcnt lgkmcnt(0)
	v_add_f32_e32 v166, v166, v167
	s_mov_b32 s100, -1
	s_mov_b32 s101, 0
	v_mov_b32_e32 v244, v166
	v_mov_b32_e32 v167, v166
	s_nop 1
	v_permlane32_swap_b32_e32 v244, v167
	v_cndmask_b32_e64 v167, v244, v167, s[100:101]
	s_and_saveexec_b64 s[48:49], s[6:7]
	s_cbranch_execz .LBB0_1420
	s_waitcnt lgkmcnt(0)
	v_add_f32_e32 v166, v166, v167
	ds_write_b32 v165, v166 offset:512
.LBB0_1420:
	s_or_b64 exec, exec, s[48:49]
	v_mul_f32_e32 v166, v103, v103
	s_waitcnt lgkmcnt(0)
	v_mul_f32_e32 v167, v105, v105
	v_fmac_f32_e32 v166, v102, v102
	v_fmac_f32_e32 v167, v104, v104
	v_add_f32_e32 v166, v166, v167
	v_mul_f32_e32 v167, v99, v99
	v_mul_f32_e32 v168, v101, v101
	v_fmac_f32_e32 v167, v98, v98
	v_fmac_f32_e32 v168, v100, v100
	v_add_f32_e32 v167, v167, v168
	v_add_f32_e32 v166, v166, v167
	s_mov_b32 s100, 0xffff
	s_mov_b32 s101, 0xffff
	v_mov_b32_e32 v244, v166
	v_mov_b32_e32 v167, v166
	s_nop 1
	v_permlane16_swap_b32_e32 v244, v167
	v_cndmask_b32_e64 v167, v244, v167, s[100:101]
	s_waitcnt lgkmcnt(0)
	v_add_f32_e32 v166, v166, v167
	s_mov_b32 s100, -1
	s_mov_b32 s101, 0
	v_mov_b32_e32 v244, v166
	v_mov_b32_e32 v167, v166
	s_nop 1
	v_permlane32_swap_b32_e32 v244, v167
	v_cndmask_b32_e64 v167, v244, v167, s[100:101]
	s_and_saveexec_b64 s[48:49], s[6:7]
	s_cbranch_execz .LBB0_1422
	s_waitcnt lgkmcnt(0)
	v_add_f32_e32 v166, v166, v167
	ds_write_b32 v165, v166 offset:1024
.LBB0_1422:
	s_or_b64 exec, exec, s[48:49]
	v_mul_f32_e32 v166, v87, v87
	s_waitcnt lgkmcnt(0)
	v_mul_f32_e32 v167, v89, v89
	v_fmac_f32_e32 v166, v86, v86
	v_fmac_f32_e32 v167, v88, v88
	v_add_f32_e32 v166, v166, v167
	v_mul_f32_e32 v167, v83, v83
	v_mul_f32_e32 v168, v85, v85
	v_fmac_f32_e32 v167, v82, v82
	v_fmac_f32_e32 v168, v84, v84
	v_add_f32_e32 v167, v167, v168
	v_add_f32_e32 v166, v166, v167
	s_mov_b32 s100, 0xffff
	s_mov_b32 s101, 0xffff
	v_mov_b32_e32 v244, v166
	v_mov_b32_e32 v167, v166
	s_nop 1
	v_permlane16_swap_b32_e32 v244, v167
	v_cndmask_b32_e64 v167, v244, v167, s[100:101]
	s_waitcnt lgkmcnt(0)
	v_add_f32_e32 v166, v166, v167
	s_mov_b32 s100, -1
	s_mov_b32 s101, 0
	v_mov_b32_e32 v244, v166
	v_mov_b32_e32 v167, v166
	s_nop 1
	v_permlane32_swap_b32_e32 v244, v167
	v_cndmask_b32_e64 v167, v244, v167, s[100:101]
	s_and_saveexec_b64 s[48:49], s[6:7]
	s_cbranch_execz .LBB0_1424
	s_waitcnt lgkmcnt(0)
	v_add_f32_e32 v166, v166, v167
	ds_write_b32 v165, v166 offset:1536
.LBB0_1424:
	s_or_b64 exec, exec, s[48:49]
	v_mul_f32_e32 v166, v111, v111
	s_waitcnt lgkmcnt(0)
	v_mul_f32_e32 v167, v113, v113
	v_fmac_f32_e32 v166, v110, v110
	v_fmac_f32_e32 v167, v112, v112
	v_add_f32_e32 v166, v166, v167
	v_mul_f32_e32 v167, v107, v107
	v_mul_f32_e32 v168, v109, v109
	v_fmac_f32_e32 v167, v106, v106
	v_fmac_f32_e32 v168, v108, v108
	v_add_f32_e32 v167, v167, v168
	v_add_f32_e32 v166, v166, v167
	s_mov_b32 s100, 0xffff
	s_mov_b32 s101, 0xffff
	v_mov_b32_e32 v244, v166
	v_mov_b32_e32 v167, v166
	s_nop 1
	v_permlane16_swap_b32_e32 v244, v167
	v_cndmask_b32_e64 v167, v244, v167, s[100:101]
	s_waitcnt lgkmcnt(0)
	v_add_f32_e32 v167, v166, v167
	s_mov_b32 s100, -1
	s_mov_b32 s101, 0
	v_mov_b32_e32 v244, v167
	v_mov_b32_e32 v168, v167
	s_nop 1
	v_permlane32_swap_b32_e32 v244, v168
	v_cndmask_b32_e64 v168, v244, v168, s[100:101]
	v_add_u32_e32 v166, s64, v155
	s_and_saveexec_b64 s[48:49], s[6:7]
	s_cbranch_execz .LBB0_1426
	s_waitcnt lgkmcnt(0)
	v_add_f32_e32 v167, v167, v168
	ds_write_b32 v166, v167
.LBB0_1426:
	s_or_b64 exec, exec, s[48:49]
	v_mul_f32_e32 v167, v95, v95
	s_waitcnt lgkmcnt(0)
	v_mul_f32_e32 v168, v97, v97
	v_fmac_f32_e32 v167, v94, v94
	v_fmac_f32_e32 v168, v96, v96
	v_add_f32_e32 v167, v167, v168
	v_mul_f32_e32 v168, v91, v91
	v_mul_f32_e32 v169, v93, v93
	v_fmac_f32_e32 v168, v90, v90
	v_fmac_f32_e32 v169, v92, v92
	v_add_f32_e32 v168, v168, v169
	v_add_f32_e32 v167, v167, v168
	s_mov_b32 s100, 0xffff
	s_mov_b32 s101, 0xffff
	v_mov_b32_e32 v244, v167
	v_mov_b32_e32 v168, v167
	s_nop 1
	v_permlane16_swap_b32_e32 v244, v168
	v_cndmask_b32_e64 v168, v244, v168, s[100:101]
	s_waitcnt lgkmcnt(0)
	v_add_f32_e32 v167, v167, v168
	s_mov_b32 s100, -1
	s_mov_b32 s101, 0
	v_mov_b32_e32 v244, v167
	v_mov_b32_e32 v168, v167
	s_nop 1
	v_permlane32_swap_b32_e32 v244, v168
	v_cndmask_b32_e64 v168, v244, v168, s[100:101]
	s_and_saveexec_b64 s[48:49], s[6:7]
	s_cbranch_execz .LBB0_1428
	s_waitcnt lgkmcnt(0)
	v_add_f32_e32 v167, v167, v168
	ds_write_b32 v166, v167 offset:512
.LBB0_1428:
	s_or_b64 exec, exec, s[48:49]
	v_mul_f32_e32 v167, v79, v79
	s_waitcnt lgkmcnt(0)
	v_mul_f32_e32 v168, v81, v81
	v_fmac_f32_e32 v167, v78, v78
	v_fmac_f32_e32 v168, v80, v80
	v_add_f32_e32 v167, v167, v168
	v_mul_f32_e32 v168, v75, v75
	v_mul_f32_e32 v169, v77, v77
	v_fmac_f32_e32 v168, v74, v74
	v_fmac_f32_e32 v169, v76, v76
	v_add_f32_e32 v168, v168, v169
	v_add_f32_e32 v167, v167, v168
	s_mov_b32 s100, 0xffff
	s_mov_b32 s101, 0xffff
	v_mov_b32_e32 v244, v167
	v_mov_b32_e32 v168, v167
	s_nop 1
	v_permlane16_swap_b32_e32 v244, v168
	v_cndmask_b32_e64 v168, v244, v168, s[100:101]
	s_waitcnt lgkmcnt(0)
	v_add_f32_e32 v167, v167, v168
	s_mov_b32 s100, -1
	s_mov_b32 s101, 0
	v_mov_b32_e32 v244, v167
	v_mov_b32_e32 v168, v167
	s_nop 1
	v_permlane32_swap_b32_e32 v244, v168
	v_cndmask_b32_e64 v168, v244, v168, s[100:101]
	s_and_saveexec_b64 s[48:49], s[6:7]
	s_cbranch_execz .LBB0_1430
	s_waitcnt lgkmcnt(0)
	v_add_f32_e32 v167, v167, v168
	ds_write_b32 v166, v167 offset:1024
.LBB0_1430:
	s_or_b64 exec, exec, s[48:49]
	v_mul_f32_e32 v167, v71, v71
	s_waitcnt lgkmcnt(0)
	v_mul_f32_e32 v168, v73, v73
	v_fmac_f32_e32 v167, v70, v70
	v_fmac_f32_e32 v168, v72, v72
	v_add_f32_e32 v167, v167, v168
	v_mul_f32_e32 v168, v67, v67
	v_mul_f32_e32 v169, v69, v69
	v_fmac_f32_e32 v168, v66, v66
	v_fmac_f32_e32 v169, v68, v68
	v_add_f32_e32 v168, v168, v169
	v_add_f32_e32 v167, v167, v168
	s_mov_b32 s100, 0xffff
	s_mov_b32 s101, 0xffff
	v_mov_b32_e32 v244, v167
	v_mov_b32_e32 v168, v167
	s_nop 1
	v_permlane16_swap_b32_e32 v244, v168
	v_cndmask_b32_e64 v168, v244, v168, s[100:101]
	s_waitcnt lgkmcnt(0)
	v_add_f32_e32 v167, v167, v168
	s_mov_b32 s100, -1
	s_mov_b32 s101, 0
	v_mov_b32_e32 v244, v167
	v_mov_b32_e32 v168, v167
	s_nop 1
	v_permlane32_swap_b32_e32 v244, v168
	v_cndmask_b32_e64 v168, v244, v168, s[100:101]
	s_and_saveexec_b64 s[48:49], s[6:7]
	s_cbranch_execz .LBB0_1432
	s_waitcnt lgkmcnt(0)
	v_add_f32_e32 v167, v167, v168
	ds_write_b32 v166, v167 offset:1536
.LBB0_1432:
	s_or_b64 exec, exec, s[48:49]
	v_mul_f32_e32 v167, v63, v63
	s_waitcnt lgkmcnt(0)
	v_mul_f32_e32 v168, v65, v65
	v_fmac_f32_e32 v167, v62, v62
	v_fmac_f32_e32 v168, v64, v64
	v_add_f32_e32 v167, v167, v168
	v_mul_f32_e32 v168, v59, v59
	v_mul_f32_e32 v169, v61, v61
	v_fmac_f32_e32 v168, v58, v58
	v_fmac_f32_e32 v169, v60, v60
	v_add_f32_e32 v168, v168, v169
	v_add_f32_e32 v167, v167, v168
	s_mov_b32 s100, 0xffff
	s_mov_b32 s101, 0xffff
	v_mov_b32_e32 v244, v167
	v_mov_b32_e32 v168, v167
	s_nop 1
	v_permlane16_swap_b32_e32 v244, v168
	v_cndmask_b32_e64 v168, v244, v168, s[100:101]
	s_waitcnt lgkmcnt(0)
	v_add_f32_e32 v167, v167, v168
	s_mov_b32 s100, -1
	s_mov_b32 s101, 0
	v_mov_b32_e32 v244, v167
	v_mov_b32_e32 v168, v167
	s_nop 1
	v_permlane32_swap_b32_e32 v244, v168
	v_cndmask_b32_e64 v168, v244, v168, s[100:101]
	s_and_saveexec_b64 s[48:49], s[6:7]
	s_cbranch_execz .LBB0_1434
	s_waitcnt lgkmcnt(0)
	v_add_f32_e32 v167, v167, v168
	ds_write_b32 v165, v167 offset:4096
.LBB0_1434:
	s_or_b64 exec, exec, s[48:49]
	v_mul_f32_e32 v167, v55, v55
	s_waitcnt lgkmcnt(0)
	v_mul_f32_e32 v168, v57, v57
	v_fmac_f32_e32 v167, v54, v54
	v_fmac_f32_e32 v168, v56, v56
	v_add_f32_e32 v167, v167, v168
	v_mul_f32_e32 v168, v51, v51
	v_mul_f32_e32 v169, v53, v53
	v_fmac_f32_e32 v168, v50, v50
	v_fmac_f32_e32 v169, v52, v52
	v_add_f32_e32 v168, v168, v169
	v_add_f32_e32 v167, v167, v168
	s_mov_b32 s100, 0xffff
	s_mov_b32 s101, 0xffff
	v_mov_b32_e32 v244, v167
	v_mov_b32_e32 v168, v167
	s_nop 1
	v_permlane16_swap_b32_e32 v244, v168
	v_cndmask_b32_e64 v168, v244, v168, s[100:101]
	s_waitcnt lgkmcnt(0)
	v_add_f32_e32 v167, v167, v168
	s_mov_b32 s100, -1
	s_mov_b32 s101, 0
	v_mov_b32_e32 v244, v167
	v_mov_b32_e32 v168, v167
	s_nop 1
	v_permlane32_swap_b32_e32 v244, v168
	v_cndmask_b32_e64 v168, v244, v168, s[100:101]
	s_and_saveexec_b64 s[48:49], s[6:7]
	s_cbranch_execz .LBB0_1436
	s_waitcnt lgkmcnt(0)
	v_add_f32_e32 v167, v167, v168
	ds_write_b32 v165, v167 offset:4608
.LBB0_1436:
	s_or_b64 exec, exec, s[48:49]
	v_mul_f32_e32 v167, v39, v39
	s_waitcnt lgkmcnt(0)
	v_mul_f32_e32 v168, v41, v41
	v_fmac_f32_e32 v167, v38, v38
	v_fmac_f32_e32 v168, v40, v40
	v_add_f32_e32 v167, v167, v168
	v_mul_f32_e32 v168, v35, v35
	v_mul_f32_e32 v169, v37, v37
	v_fmac_f32_e32 v168, v34, v34
	v_fmac_f32_e32 v169, v36, v36
	v_add_f32_e32 v168, v168, v169
	v_add_f32_e32 v167, v167, v168
	s_mov_b32 s100, 0xffff
	s_mov_b32 s101, 0xffff
	v_mov_b32_e32 v244, v167
	v_mov_b32_e32 v168, v167
	s_nop 1
	v_permlane16_swap_b32_e32 v244, v168
	v_cndmask_b32_e64 v168, v244, v168, s[100:101]
	s_waitcnt lgkmcnt(0)
	v_add_f32_e32 v167, v167, v168
	s_mov_b32 s100, -1
	s_mov_b32 s101, 0
	v_mov_b32_e32 v244, v167
	v_mov_b32_e32 v168, v167
	s_nop 1
	v_permlane32_swap_b32_e32 v244, v168
	v_cndmask_b32_e64 v168, v244, v168, s[100:101]
	s_and_saveexec_b64 s[48:49], s[6:7]
	s_cbranch_execz .LBB0_1438
	s_waitcnt lgkmcnt(0)
	v_add_f32_e32 v167, v167, v168
	ds_write_b32 v165, v167 offset:5120
.LBB0_1438:
	s_or_b64 exec, exec, s[48:49]
	v_mul_f32_e32 v167, v23, v23
	s_waitcnt lgkmcnt(0)
	v_mul_f32_e32 v168, v25, v25
	v_fmac_f32_e32 v167, v22, v22
	v_fmac_f32_e32 v168, v24, v24
	v_add_f32_e32 v167, v167, v168
	v_mul_f32_e32 v168, v19, v19
	v_mul_f32_e32 v169, v21, v21
	v_fmac_f32_e32 v168, v18, v18
	v_fmac_f32_e32 v169, v20, v20
	v_add_f32_e32 v168, v168, v169
	v_add_f32_e32 v167, v167, v168
	s_mov_b32 s100, 0xffff
	s_mov_b32 s101, 0xffff
	v_mov_b32_e32 v244, v167
	v_mov_b32_e32 v168, v167
	s_nop 1
	v_permlane16_swap_b32_e32 v244, v168
	v_cndmask_b32_e64 v168, v244, v168, s[100:101]
	s_waitcnt lgkmcnt(0)
	v_add_f32_e32 v167, v167, v168
	s_mov_b32 s100, -1
	s_mov_b32 s101, 0
	v_mov_b32_e32 v244, v167
	v_mov_b32_e32 v168, v167
	s_nop 1
	v_permlane32_swap_b32_e32 v244, v168
	v_cndmask_b32_e64 v168, v244, v168, s[100:101]
	s_and_saveexec_b64 s[48:49], s[6:7]
	s_cbranch_execz .LBB0_1440
	s_waitcnt lgkmcnt(0)
	v_add_f32_e32 v167, v167, v168
	ds_write_b32 v165, v167 offset:5632
.LBB0_1440:
	s_or_b64 exec, exec, s[48:49]
	v_mul_f32_e32 v165, v47, v47
	v_mul_f32_e32 v167, v49, v49
	v_fmac_f32_e32 v165, v46, v46
	v_fmac_f32_e32 v167, v48, v48
	v_add_f32_e32 v165, v165, v167
	v_mul_f32_e32 v167, v43, v43
	s_waitcnt lgkmcnt(0)
	v_mul_f32_e32 v168, v45, v45
	v_fmac_f32_e32 v167, v42, v42
	v_fmac_f32_e32 v168, v44, v44
	v_add_f32_e32 v167, v167, v168
	v_add_f32_e32 v165, v165, v167
	s_mov_b32 s100, 0xffff
	s_mov_b32 s101, 0xffff
	v_mov_b32_e32 v244, v165
	v_mov_b32_e32 v167, v165
	s_nop 1
	v_permlane16_swap_b32_e32 v244, v167
	v_cndmask_b32_e64 v167, v244, v167, s[100:101]
	s_waitcnt lgkmcnt(0)
	v_add_f32_e32 v165, v165, v167
	s_mov_b32 s100, -1
	s_mov_b32 s101, 0
	v_mov_b32_e32 v244, v165
	v_mov_b32_e32 v167, v165
	s_nop 1
	v_permlane32_swap_b32_e32 v244, v167
	v_cndmask_b32_e64 v167, v244, v167, s[100:101]
	s_and_saveexec_b64 s[48:49], s[6:7]
	s_cbranch_execz .LBB0_1442
	s_waitcnt lgkmcnt(0)
	v_add_f32_e32 v165, v165, v167
	ds_write_b32 v166, v165 offset:4096
.LBB0_1442:
	s_or_b64 exec, exec, s[48:49]
	v_mul_f32_e32 v165, v31, v31
	s_waitcnt lgkmcnt(0)
	v_mul_f32_e32 v167, v33, v33
	v_fmac_f32_e32 v165, v30, v30
	v_fmac_f32_e32 v167, v32, v32
	v_add_f32_e32 v165, v165, v167
	v_mul_f32_e32 v167, v27, v27
	v_mul_f32_e32 v168, v29, v29
	v_fmac_f32_e32 v167, v26, v26
	v_fmac_f32_e32 v168, v28, v28
	v_add_f32_e32 v167, v167, v168
	v_add_f32_e32 v165, v165, v167
	s_mov_b32 s100, 0xffff
	s_mov_b32 s101, 0xffff
	v_mov_b32_e32 v244, v165
	v_mov_b32_e32 v167, v165
	s_nop 1
	v_permlane16_swap_b32_e32 v244, v167
	v_cndmask_b32_e64 v167, v244, v167, s[100:101]
	s_waitcnt lgkmcnt(0)
	v_add_f32_e32 v165, v165, v167
	s_mov_b32 s100, -1
	s_mov_b32 s101, 0
	v_mov_b32_e32 v244, v165
	v_mov_b32_e32 v167, v165
	s_nop 1
	v_permlane32_swap_b32_e32 v244, v167
	v_cndmask_b32_e64 v167, v244, v167, s[100:101]
	s_and_saveexec_b64 s[48:49], s[6:7]
	s_cbranch_execz .LBB0_1444
	s_waitcnt lgkmcnt(0)
	v_add_f32_e32 v165, v165, v167
	ds_write_b32 v166, v165 offset:4608
.LBB0_1444:
	s_or_b64 exec, exec, s[48:49]
	v_mul_f32_e32 v165, v15, v15
	s_waitcnt lgkmcnt(0)
	v_mul_f32_e32 v167, v17, v17
	v_fmac_f32_e32 v165, v14, v14
	v_fmac_f32_e32 v167, v16, v16
	v_add_f32_e32 v165, v165, v167
	v_mul_f32_e32 v167, v11, v11
	v_mul_f32_e32 v168, v13, v13
	v_fmac_f32_e32 v167, v10, v10
	v_fmac_f32_e32 v168, v12, v12
	v_add_f32_e32 v167, v167, v168
	v_add_f32_e32 v165, v165, v167
	s_mov_b32 s100, 0xffff
	s_mov_b32 s101, 0xffff
	v_mov_b32_e32 v244, v165
	v_mov_b32_e32 v167, v165
	s_nop 1
	v_permlane16_swap_b32_e32 v244, v167
	v_cndmask_b32_e64 v167, v244, v167, s[100:101]
	s_waitcnt lgkmcnt(0)
	v_add_f32_e32 v165, v165, v167
	s_mov_b32 s100, -1
	s_mov_b32 s101, 0
	v_mov_b32_e32 v244, v165
	v_mov_b32_e32 v167, v165
	s_nop 1
	v_permlane32_swap_b32_e32 v244, v167
	v_cndmask_b32_e64 v167, v244, v167, s[100:101]
	s_and_saveexec_b64 s[48:49], s[6:7]
	s_cbranch_execz .LBB0_1446
	s_waitcnt lgkmcnt(0)
	v_add_f32_e32 v165, v165, v167
	ds_write_b32 v166, v165 offset:5120
.LBB0_1446:
	s_or_b64 exec, exec, s[48:49]
	v_mul_f32_e32 v165, v7, v7
	s_waitcnt lgkmcnt(0)
	v_mul_f32_e32 v167, v9, v9
	v_fmac_f32_e32 v165, v6, v6
	v_fmac_f32_e32 v167, v8, v8
	v_add_f32_e32 v165, v165, v167
	v_mul_f32_e32 v167, v3, v3
	v_mul_f32_e32 v168, v5, v5
	v_fmac_f32_e32 v167, v2, v2
	v_fmac_f32_e32 v168, v4, v4
	v_add_f32_e32 v167, v167, v168
	v_add_f32_e32 v165, v165, v167
	s_mov_b32 s100, 0xffff
	s_mov_b32 s101, 0xffff
	v_mov_b32_e32 v244, v165
	v_mov_b32_e32 v163, v165
	s_nop 1
	v_permlane16_swap_b32_e32 v244, v163
	v_cndmask_b32_e64 v163, v244, v163, s[100:101]
	s_waitcnt lgkmcnt(0)
	v_add_f32_e32 v163, v165, v163
	s_mov_b32 s100, -1
	s_mov_b32 s101, 0
	v_mov_b32_e32 v244, v163
	v_mov_b32_e32 v164, v163
	s_nop 1
	v_permlane32_swap_b32_e32 v244, v164
	v_cndmask_b32_e64 v164, v244, v164, s[100:101]
	s_and_saveexec_b64 s[48:49], s[6:7]
	s_cbranch_execz .LBB0_1448
	s_waitcnt lgkmcnt(0)
	v_add_f32_e32 v163, v163, v164
	ds_write_b32 v166, v163 offset:5632
